# speedup vs baseline: 1.0214x; 1.0214x over previous
_Z8k_stageAPKfS0_S0_S0_PDF16_PKDF16_S0_S1_ii:
	v_readfirstlane_b32 s94, v0
	s_nop 0
	s_lshr_b32 s94, s94, 6
	s_cmp_lt_u32 s94, 4
	s_cbranch_scc1 .Lmyprio1
	s_setprio 1
.Lmyprio1:
	s_load_dwordx8 s[4:11], s[0:1], 0x0
	v_readfirstlane_b32 s14, v0
	s_lshr_b32 s15, s2, 5
	s_lshl_b32 s2, s2, 7
	s_lshr_b32 s20, s14, 6
	s_and_b32 s12, s2, 0xf80
	s_lshl_b32 s13, s15, 12
	s_mov_b32 s18, s3
	s_cmpk_lt_u32 s14, 0x100
	s_waitcnt lgkmcnt(0)
	s_cselect_b32 s2, s4, s6
	s_cselect_b32 s3, s5, s7
	s_cselect_b32 s4, s8, s10
	s_cselect_b32 s5, s9, s11
	s_cmp_eq_u32 s18, 0
	s_cselect_b32 s3, s3, s5
	s_cselect_b32 s2, s2, s4
	s_lshr_b32 s5, s14, 1
	s_lshl_b32 s4, s15, 7
	s_and_b32 s5, s5, 0x60
	v_bfe_u32 v1, v0, 5, 1
	s_or_b32 s4, s5, s4
	v_lshl_or_b32 v82, v1, 3, s4
	v_mov_b32_e32 v83, 0
	v_lshlrev_b64 v[2:3], 14, v[82:83]
	v_lshlrev_b32_e32 v78, 2, v0
	s_mov_b32 s17, 0
	v_lshl_add_u64 v[2:3], s[2:3], 0, v[2:3]
	s_lshl_b32 s16, s12, 2
	v_and_b32_e32 v79, 0x7c, v78
	v_lshl_add_u64 v[2:3], v[2:3], 0, s[16:17]
	v_lshlrev_b32_e32 v82, 2, v79
	v_lshl_add_u64 v[42:43], v[2:3], 0, v[82:83]
	s_movk_i32 s21, 0x4000
	v_add_co_u32_e32 v10, vcc, s21, v42
	s_mov_b32 s2, 0x8000
	s_nop 0
	v_addc_co_u32_e32 v11, vcc, 0, v43, vcc
	v_add_co_u32_e32 v18, vcc, s2, v42
	s_mov_b32 s2, 0xc000
	s_nop 0
	v_addc_co_u32_e32 v19, vcc, 0, v43, vcc
	v_add_co_u32_e32 v20, vcc, s2, v42
	s_mov_b32 s14, 0x10000
	s_nop 0
	v_addc_co_u32_e32 v21, vcc, 0, v43, vcc
	v_add_co_u32_e32 v26, vcc, s14, v42
	s_mov_b32 s2, 0x14000
	s_nop 0
	v_addc_co_u32_e32 v27, vcc, 0, v43, vcc
	v_add_co_u32_e32 v28, vcc, s2, v42
	s_mov_b32 s2, 0x18000
	s_nop 0
	v_addc_co_u32_e32 v29, vcc, 0, v43, vcc
	v_add_co_u32_e32 v34, vcc, s2, v42
	s_mov_b32 s2, 0x1c000
	s_nop 0
	v_addc_co_u32_e32 v35, vcc, 0, v43, vcc
	v_add_co_u32_e32 v36, vcc, s2, v42
	s_mov_b32 s2, 0x40000
	s_nop 0
	v_addc_co_u32_e32 v37, vcc, 0, v43, vcc
	v_add_co_u32_e32 v66, vcc, s2, v42
	s_mov_b32 s2, 0x44000
	s_nop 0
	v_addc_co_u32_e32 v67, vcc, 0, v43, vcc
	v_add_co_u32_e32 v68, vcc, s2, v42
	s_mov_b32 s2, 0x48000
	s_nop 0
	v_addc_co_u32_e32 v69, vcc, 0, v43, vcc
	global_load_dwordx4 v[2:5], v[42:43], off nt
	global_load_dwordx4 v[6:9], v[10:11], off nt
	v_add_co_u32_e32 v44, vcc, s2, v42
	global_load_dwordx4 v[10:13], v[18:19], off nt
	global_load_dwordx4 v[14:17], v[20:21], off nt
	s_nop 0
	global_load_dwordx4 v[18:21], v[26:27], off nt
	global_load_dwordx4 v[22:25], v[28:29], off nt
	s_nop 0
	global_load_dwordx4 v[26:29], v[34:35], off nt
	global_load_dwordx4 v[30:33], v[36:37], off nt
	v_addc_co_u32_e32 v45, vcc, 0, v43, vcc
	s_mov_b32 s2, 0x4c000
	v_add_co_u32_e32 v46, vcc, s2, v42
	s_mov_b32 s2, 0x50000
	s_nop 0
	v_addc_co_u32_e32 v47, vcc, 0, v43, vcc
	v_add_co_u32_e32 v70, vcc, s2, v42
	s_mov_b32 s2, 0x54000
	s_nop 0
	v_addc_co_u32_e32 v71, vcc, 0, v43, vcc
	v_add_co_u32_e32 v72, vcc, s2, v42
	s_mov_b32 s2, 0x58000
	s_nop 0
	v_addc_co_u32_e32 v73, vcc, 0, v43, vcc
	v_add_co_u32_e32 v74, vcc, s2, v42
	s_mov_b32 s2, 0x5c000
	s_nop 0
	v_addc_co_u32_e32 v75, vcc, 0, v43, vcc
	v_add_co_u32_e32 v76, vcc, s2, v42
	global_load_dwordx4 v[34:37], v[44:45], off nt
	global_load_dwordx4 v[38:41], v[46:47], off nt
	v_addc_co_u32_e32 v77, vcc, 0, v43, vcc
	global_load_dwordx4 v[42:45], v[74:75], off nt
	global_load_dwordx4 v[46:49], v[76:77], off nt
	global_load_dwordx4 v[50:53], v[70:71], off nt
	global_load_dwordx4 v[54:57], v[72:73], off nt
	global_load_dwordx4 v[58:61], v[66:67], off nt
	global_load_dwordx4 v[62:65], v[68:69], off nt
	v_lshl_or_b32 v1, s20, 2, v1
	v_lshrrev_b32_e32 v70, 5, v0
	v_or_b32_e32 v141, 0x200, v0
	v_or_b32_e32 v142, 0x600, v0
	s_or_b32 s16, s13, s12
	s_ashr_i32 s19, s18, 31
	s_lshl_b64 s[12:13], s[16:17], 9
	s_mov_b32 s15, 0x20000
	v_or_b32_e32 v144, 0xa00, v0
	v_bfe_u32 v140, v0, 4, 2
	v_and_b32_e32 v145, 15, v0
	v_lshlrev_b32_e32 v220, 9, v145
	s_waitcnt vmcnt(14)
	v_cvt_pk_f16_f32 v66, v2, v6
	v_lshlrev_b32_e32 v6, 9, v79
	v_bitop3_b32 v2, v78, v1, 12 bitop3:0x6c
	s_waitcnt vmcnt(12)
	v_cvt_pk_f16_f32 v67, v10, v14
	s_waitcnt vmcnt(10)
	v_cvt_pk_f16_f32 v68, v18, v22
	s_waitcnt vmcnt(8)
	v_cvt_pk_f16_f32 v69, v26, v30
	v_lshl_add_u32 v2, v2, 4, v6
	ds_write_b128 v2, v[66:69]
	v_cvt_pk_f16_f32 v66, v3, v7
	v_or_b32_e32 v7, 1, v79
	v_lshlrev_b32_e32 v10, 9, v7
	v_bitop3_b32 v2, v7, v1, 13 bitop3:0x6c
	v_cvt_pk_f16_f32 v69, v27, v31
	v_cvt_pk_f16_f32 v68, v19, v23
	v_cvt_pk_f16_f32 v67, v11, v15
	v_lshl_add_u32 v2, v2, 4, v10
	ds_write_b128 v2, v[66:69]
	v_cvt_pk_f16_f32 v66, v4, v8
	v_or_b32_e32 v8, 2, v79
	v_lshlrev_b32_e32 v11, 9, v8
	v_bitop3_b32 v2, v8, v1, 14 bitop3:0x6c
	v_cvt_pk_f16_f32 v69, v28, v32
	v_cvt_pk_f16_f32 v68, v20, v24
	v_cvt_pk_f16_f32 v67, v12, v16
	v_lshl_add_u32 v2, v2, 4, v11
	v_cvt_pk_f16_f32 v12, v5, v9
	v_or_b32_e32 v9, 3, v79
	ds_write_b128 v2, v[66:69]
	v_lshlrev_b32_e32 v16, 9, v9
	v_bitop3_b32 v2, v9, v1, 15 bitop3:0x6c
	v_cvt_pk_f16_f32 v15, v29, v33
	v_cvt_pk_f16_f32 v14, v21, v25
	v_cvt_pk_f16_f32 v13, v13, v17
	v_lshl_add_u32 v2, v2, 4, v16
	v_or_b32_e32 v1, 2, v1
	ds_write_b128 v2, v[12:15]
	v_bitop3_b32 v12, v78, v1, 12 bitop3:0x6c
	s_waitcnt vmcnt(4)
	v_cvt_pk_f16_f32 v5, v42, v46
	s_waitcnt vmcnt(2)
	v_cvt_pk_f16_f32 v4, v50, v54
	v_cvt_pk_f16_f32 v3, v34, v38
	s_waitcnt vmcnt(0)
	v_cvt_pk_f16_f32 v2, v58, v62
	v_lshl_add_u32 v6, v12, 4, v6
	ds_write_b128 v6, v[2:5]
	v_bitop3_b32 v6, v7, v1, 13 bitop3:0x6c
	v_cvt_pk_f16_f32 v5, v43, v47
	v_cvt_pk_f16_f32 v4, v51, v55
	v_cvt_pk_f16_f32 v3, v35, v39
	v_cvt_pk_f16_f32 v2, v59, v63
	v_lshl_add_u32 v6, v6, 4, v10
	ds_write_b128 v6, v[2:5]
	v_bitop3_b32 v6, v8, v1, 14 bitop3:0x6c
	v_cvt_pk_f16_f32 v5, v44, v48
	v_cvt_pk_f16_f32 v4, v52, v56
	v_cvt_pk_f16_f32 v3, v36, v40
	v_cvt_pk_f16_f32 v2, v60, v64
	v_lshl_add_u32 v6, v6, 4, v11
	v_bitop3_b32 v1, v9, v1, 15 bitop3:0x6c
	ds_write_b128 v6, v[2:5]
	v_cvt_pk_f16_f32 v5, v45, v49
	v_cvt_pk_f16_f32 v4, v53, v57
	v_cvt_pk_f16_f32 v3, v37, v41
	v_cvt_pk_f16_f32 v2, v61, v65
	v_lshl_add_u32 v1, v1, 4, v16
	ds_write_b128 v1, v[2:5]
	v_bitop3_b32 v2, v70, v0, 31 bitop3:0x78
	v_lshlrev_b32_e32 v1, 9, v70
	v_lshlrev_b32_e32 v22, 4, v2
	v_or_b32_e32 v10, v22, v1
	s_waitcnt lgkmcnt(0)
	s_barrier
	ds_read_b128 v[2:5], v10
	s_load_dwordx8 s[4:11], s[0:1], 0x20
	s_load_dwordx2 s[2:3], s[0:1], 0x40
	v_lshlrev_b32_e32 v24, 4, v0
	v_and_b32_e32 v25, 0x1e00, v24
	v_or_b32_e32 v26, v22, v25
	s_waitcnt lgkmcnt(0)
	v_pk_max_f16 v6, v5, v5
	v_and_b32_e32 v18, 31, v0
	v_pk_max_f16 v9, v6, 0
	v_pk_max_f16 v6, v4, v4
	v_lshlrev_b32_e32 v29, 4, v18
	v_pk_max_f16 v8, v6, 0
	v_pk_max_f16 v6, v3, v3
	s_lshl_b64 s[0:1], s[18:19], 23
	v_pk_max_f16 v7, v6, 0
	v_pk_max_f16 v6, v2, v2
	s_add_u32 s0, s4, s0
	v_pk_max_f16 v6, v6, 0
	ds_write_b128 v10, v[6:9]
	v_lshlrev_b32_e32 v6, 4, v141
	v_and_b32_e32 v23, 0x3e00, v6
	v_or_b32_e32 v14, v22, v23
	ds_read_b128 v[6:9], v14
	s_addc_u32 s1, s5, s1
	s_add_u32 s12, s0, s12
	s_addc_u32 s0, s1, s13
	s_and_b32 s13, s0, 0xffff
	s_waitcnt lgkmcnt(0)
	v_pk_max_f16 v10, v9, v9
	v_or_b32_e32 v1, v1, v29
	v_pk_max_f16 v13, v10, 0
	v_pk_max_f16 v10, v8, v8
	buffer_store_dwordx4 v[2:5], v1, s[12:15], 0 offen sc1
	v_pk_max_f16 v12, v10, 0
	v_pk_max_f16 v10, v7, v7
	v_or_b32_e32 v1, v23, v29
	v_pk_max_f16 v11, v10, 0
	v_pk_max_f16 v10, v6, v6
	buffer_store_dwordx4 v[6:9], v1, s[12:15], 0 offen sc1
	v_pk_max_f16 v10, v10, 0
	ds_write_b128 v14, v[10:13]
	ds_read_b128 v[10:13], v26 offset:16384
	v_or_b32_e32 v25, v25, v29
	v_or_b32_e32 v6, 0x4000, v25
	s_mov_b32 s0, 0xfe00
	s_waitcnt lgkmcnt(0)
	v_pk_max_f16 v14, v13, v13
	s_nop 0
	v_pk_max_f16 v17, v14, 0
	v_pk_max_f16 v14, v12, v12
	buffer_store_dwordx4 v[10:13], v6, s[12:15], 0 offen sc1
	v_pk_max_f16 v16, v14, 0
	v_pk_max_f16 v14, v11, v11
	s_nop 0
	v_pk_max_f16 v15, v14, 0
	v_pk_max_f16 v14, v10, v10
	s_nop 0
	v_pk_max_f16 v14, v14, 0
	ds_write_b128 v26, v[14:17] offset:16384
	v_lshlrev_b32_e32 v14, 4, v142
	v_and_b32_e32 v27, 0x7e00, v14
	v_or_b32_e32 v28, v22, v27
	ds_read_b128 v[14:17], v28
	v_or_b32_e32 v10, v27, v29
	s_waitcnt lgkmcnt(0)
	v_pk_max_f16 v18, v17, v17
	s_nop 0
	v_pk_max_f16 v21, v18, 0
	v_pk_max_f16 v18, v16, v16
	buffer_store_dwordx4 v[14:17], v10, s[12:15], 0 offen sc1
	v_pk_max_f16 v20, v18, 0
	v_pk_max_f16 v18, v15, v15
	v_or_b32_e32 v10, 0x8000, v25
	v_pk_max_f16 v19, v18, 0
	v_pk_max_f16 v18, v14, v14
	s_nop 0
	v_pk_max_f16 v18, v18, 0
	ds_write_b128 v28, v[18:21]
	ds_read_b128 v[18:21], v26 offset:32768
	s_waitcnt lgkmcnt(0)
	v_pk_max_f16 v1, v21, v21
	s_nop 0
	v_pk_max_f16 v5, v1, 0
	v_pk_max_f16 v1, v20, v20
	buffer_store_dwordx4 v[18:21], v10, s[12:15], 0 offen sc1
	v_pk_max_f16 v4, v1, 0
	v_pk_max_f16 v1, v19, v19
	s_nop 0
	v_pk_max_f16 v3, v1, 0
	v_pk_max_f16 v1, v18, v18
	s_nop 0
	v_pk_max_f16 v2, v1, 0
	v_lshlrev_b32_e32 v1, 4, v144
	v_and_b32_e32 v1, 0xbe00, v1
	ds_write_b128 v26, v[2:5] offset:32768
	v_or_b32_e32 v23, v22, v1
	ds_read_b128 v[2:5], v23
	v_or_b32_e32 v1, v1, v29
	s_waitcnt lgkmcnt(0)
	v_pk_max_f16 v6, v5, v5
	s_nop 0
	v_pk_max_f16 v9, v6, 0
	v_pk_max_f16 v6, v4, v4
	buffer_store_dwordx4 v[2:5], v1, s[12:15], 0 offen sc1
	v_pk_max_f16 v8, v6, 0
	v_pk_max_f16 v6, v3, v3
	v_or_b32_e32 v1, 0xc000, v25
	v_pk_max_f16 v7, v6, 0
	v_pk_max_f16 v6, v2, v2
	s_nop 0
	v_pk_max_f16 v6, v6, 0
	ds_write_b128 v23, v[6:9]
	ds_read_b128 v[6:9], v26 offset:49152
	s_waitcnt lgkmcnt(0)
	v_pk_max_f16 v10, v9, v9
	s_nop 0
	v_pk_max_f16 v13, v10, 0
	v_pk_max_f16 v10, v8, v8
	buffer_store_dwordx4 v[6:9], v1, s[12:15], 0 offen sc1
	v_pk_max_f16 v12, v10, 0
	v_pk_max_f16 v10, v7, v7
	s_nop 0
	v_pk_max_f16 v11, v10, 0
	v_pk_max_f16 v10, v6, v6
	s_nop 0
	v_pk_max_f16 v10, v10, 0
	ds_write_b128 v26, v[10:13] offset:49152
	v_mov_b32_e32 v10, 0xe000
	v_bitop3_b32 v14, v24, s0, v10 bitop3:0xc8
	s_mul_i32 s0, s3, s18
	v_or_b32_e32 v15, v22, v14
	s_add_i32 s0, s0, s2
	ds_read_b128 v[10:13], v15
	s_mul_i32 s2, s0, 0x60000
	s_mul_hi_i32 s1, s0, 0x60000
	s_add_u32 s2, s6, s2
	s_mulk_i32 s0, 0x300
	s_addc_u32 s3, s7, s1
	s_ashr_i32 s1, s0, 31
	s_lshl_b64 s[0:1], s[0:1], 2
	v_or_b32_e32 v1, v14, v29
	s_add_u32 s4, s8, s0
	s_waitcnt lgkmcnt(0)
	buffer_store_dwordx4 v[10:13], v1, s[12:15], 0 offen sc1
	v_pk_max_f16 v1, v13, v13
	s_addc_u32 s5, s9, s1
	s_mul_i32 s0, s18, 0x1800000
	v_pk_max_f16 v5, v1, 0
	v_pk_max_f16 v1, v12, v12
	s_mul_hi_i32 s1, s18, 0x1800000
	s_add_u32 s0, s10, s0
	v_pk_max_f16 v4, v1, 0
	v_pk_max_f16 v1, v11, v11
	s_addc_u32 s1, s11, s1
	v_pk_max_f16 v3, v1, 0
	v_pk_max_f16 v1, v10, v10
	s_and_b32 s1, s1, 0xffff
	s_mul_i32 s7, s20, 0x6000
	v_pk_max_f16 v2, v1, 0
	v_and_b32_e32 v1, 63, v0
	s_mul_hi_u32 s6, s20, 0x6000
	s_add_u32 s2, s2, s7
	s_addc_u32 s3, s3, s6
	v_lshlrev_b32_e32 v82, 4, v1
	v_lshl_add_u64 v[118:119], s[2:3], 0, v[82:83]
	s_movk_i32 s6, 0x1000
	v_add_co_u32_e32 v50, vcc, s6, v118
	s_movk_i32 s6, 0x2000
	s_nop 0
	v_addc_co_u32_e32 v51, vcc, 0, v119, vcc
	ds_write_b128 v15, v[2:5]
	v_add_co_u32_e32 v52, vcc, s6, v118
	global_load_dwordx4 v[2:5], v82, s[2:3] offset:1024
	global_load_dwordx4 v[6:9], v82, s[2:3] offset:2048
	v_addc_co_u32_e32 v53, vcc, 0, v119, vcc
	global_load_dwordx4 v[10:13], v82, s[2:3] offset:3072
	global_load_dwordx4 v[14:17], v[52:53], off offset:-4096
	global_load_dwordx4 v[18:21], v[50:51], off offset:1024
	global_load_dwordx4 v[22:25], v[50:51], off offset:2048
	global_load_dwordx4 v[26:29], v82, s[2:3]
	global_load_dwordx4 v[30:33], v[50:51], off offset:3072
	global_load_dwordx4 v[34:37], v[52:53], off
	global_load_dwordx4 v[38:41], v[52:53], off offset:1024
	global_load_dwordx4 v[42:45], v[52:53], off offset:2048
	global_load_dwordx4 v[46:49], v[52:53], off offset:3072
	s_movk_i32 s2, 0x3000
	v_add_co_u32_e32 v116, vcc, s2, v118
	s_waitcnt lgkmcnt(0)
	s_nop 0
	v_addc_co_u32_e32 v117, vcc, 0, v119, vcc
	v_add_co_u32_e32 v132, vcc, s21, v118
	s_barrier
	s_cmp_lt_u32 s94, 4
	s_cbranch_scc1 .Lmystag1_2
	s_sleep 7

_Z7k_stageILi0ELi8EEv8AttnArgsPKDF16_PKfPDF16_iii:
	v_readfirstlane_b32 s94, v0
	s_nop 0
	s_lshr_b32 s94, s94, 6
	s_cmp_lt_u32 s94, 4
	s_cbranch_scc1 .Lmyprio3
	s_setprio 1
.Lmyprio3:
	s_load_dwordx4 s[8:11], s[0:1], 0x88
	s_lshl_b32 s4, s2, 4
	s_and_b32 s4, s4, 0x70
	s_lshr_b32 s5, s2, 3
	s_add_i32 s4, s4, s5
	s_lshr_b32 s7, s4, 5
	s_lshl_b32 s6, s4, 1
	s_waitcnt lgkmcnt(0)
	s_lshl_b32 s11, s2, 1
	s_cmp_gt_i32 s10, 0
	v_readfirstlane_b32 s24, v0
	s_cbranch_scc1 .LBB3_2
	s_lshl_b32 s31, s7, 12
	s_ashr_i32 s2, s3, 31
	s_mov_b64 s[4:5], 0
	s_branch .LBB3_3

_Z7k_stageILi1ELi4EEv8AttnArgsPKDF16_PKfPDF16_iii:
	v_readfirstlane_b32 s94, v0
	s_nop 0
	s_lshr_b32 s94, s94, 6
	s_cmp_lt_u32 s94, 4
	s_cbranch_scc1 .Lmyprio4
	s_setprio 1
.Lmyprio4:
	s_load_dwordx4 s[28:31], s[0:1], 0x70
	s_load_dwordx2 s[24:25], s[0:1], 0x80
	s_load_dword s33, s[0:1], 0x90
	s_lshl_b32 s4, s2, 5
	s_and_b32 s45, s4, 0xe0
	s_lshr_b32 s4, s2, 3
	s_add_i32 s45, s45, s4
	s_and_b32 s44, s2, 56
	v_readfirstlane_b32 s3, v0
	v_and_b32_e32 v1, 15, v0
	s_waitcnt lgkmcnt(0)
	s_cmp_lt_i32 s33, 1
	v_bfe_u32 v167, v0, 4, 2
	s_cbranch_scc1 .LBB4_155
	s_lshr_b32 s2, s3, 2
	v_lshrrev_b32_e32 v7, 7, v0
	v_lshrrev_b32_e32 v2, 5, v0
	v_lshrrev_b32_e32 v3, 4, v0
	s_and_b32 s2, s2, 16
	v_lshrrev_b32_e32 v4, 6, v0
	v_and_b32_e32 v7, 1, v7
	v_and_b32_e32 v2, 4, v2
	v_or_b32_e32 v179, s2, v1
	v_and_b32_e32 v5, 4, v4
	s_load_dwordx2 s[40:41], s[0:1], 0x60
	s_bitcmp1_b32 s3, 6
	v_lshlrev_b16_e32 v7, 2, v7
	v_and_b32_e32 v8, 3, v3
	s_load_dwordx4 s[36:39], s[0:1], 0x0
	s_load_dwordx2 s[4:5], s[0:1], 0x10
	s_load_dwordx8 s[8:15], s[0:1], 0x18
	s_load_dwordx2 s[6:7], s[0:1], 0x38
	s_load_dwordx8 s[16:23], s[0:1], 0x40
	v_or_b32_e32 v178, v2, v167
	v_and_or_b32 v180, s45, 56, v5
	s_cselect_b64 s[26:27], -1, 0
	s_and_b32 s3, s45, 0x3ffffc0
	v_bitop3_b16 v3, v7, v3, 3 bitop3:0xf8
	v_bitop3_b16 v7, v7, 8, v8 bitop3:0xfe
	v_lshlrev_b32_e32 v8, 12, v5
	v_bitop3_b32 v2, v2, v179, v167 bitop3:0x36
	v_or_b32_e32 v6, s3, v180
	s_and_b32 s3, s45, 0x1ffc0
	v_and_b32_e32 v3, 0xffff, v3
	v_lshl_or_b32 v184, v2, 4, v8
	v_lshlrev_b32_e32 v2, 3, v5
	v_mov_b32_e32 v169, 0
	v_lshlrev_b32_e32 v168, 5, v179
	v_lshlrev_b32_e32 v181, 6, v6
	v_or_b32_e32 v6, s3, v180
	v_and_b32_e32 v7, 0xffff, v7
	v_or_b32_e32 v186, 8, v2
	v_or_b32_e32 v188, 16, v2
	v_bitop3_b32 v2, s2, v3, v1 bitop3:0x36
	v_lshlrev_b32_e32 v166, 3, v179
	s_waitcnt lgkmcnt(0)
	v_lshl_add_u64 v[170:171], s[38:39], 0, v[168:169]
	s_mov_b32 s39, 0x20000
	v_lshlrev_b32_e32 v189, 4, v2
	v_bitop3_b32 v2, s2, v7, v1 bitop3:0x36
	v_lshlrev_b32_e32 v193, 15, v6
	v_lshl_add_u64 v[172:173], s[4:5], 0, v[168:169]
	s_and_b32 s37, s37, 0xffff
	s_mov_b32 s38, 0x1800000
	v_add_u32_e32 v182, -1, v180
	v_add_u32_e32 v183, 4, v180
	v_lshl_add_u64 v[174:175], s[14:15], 0, v[168:169]
	v_lshl_add_u64 v[176:177], s[6:7], 0, v[168:169]
	s_and_b32 s13, s13, 0xffff
	s_mov_b32 s42, 0x800000
	s_mov_b32 s43, s39
	s_and_b32 s41, s41, 0xffff
	v_or_b32_e32 v185, 64, v181
	v_or_b32_e32 v187, 0x80, v181
	v_or_b32_e32 v190, 0xc0, v181
	v_lshl_or_b32 v191, v4, 3, 24
	v_lshlrev_b32_e32 v192, 4, v2
	v_lshlrev_b32_e32 v194, 4, v179
	v_or_b32_e32 v195, 0x8000, v193
	v_or_b32_e32 v196, 0x10000, v193
	v_or_b32_e32 v197, 0x18000, v193
	s_mov_b32 s46, 0
	s_movk_i32 s47, 0x300
	v_lshlrev_b32_e32 v198, 1, v166
	s_branch .LBB4_4

_Z7k_stageILi0ELi4EEv8AttnArgsPKDF16_PKfPDF16_iii:
	v_readfirstlane_b32 s94, v0
	s_nop 0
	s_lshr_b32 s94, s94, 6
	s_cmp_lt_u32 s94, 4
	s_cbranch_scc1 .Lmyprio5
	s_setprio 1
.Lmyprio5:
	s_load_dwordx4 s[8:11], s[0:1], 0x70
	s_load_dwordx2 s[20:21], s[0:1], 0x80
	s_load_dwordx4 s[12:15], s[0:1], 0x88
	s_lshl_b32 s5, s2, 5
	s_waitcnt lgkmcnt(0)
	s_and_b32 s15, s5, 0xe0
	s_lshr_b32 s5, s2, 3
	s_add_i32 s15, s15, s5
	s_and_b32 s2, s2, 56
	v_readfirstlane_b32 s4, v0
	v_and_b32_e32 v1, 15, v0
	s_cmp_lt_i32 s14, 1
	v_bfe_u32 v158, v0, 4, 2
	s_cbranch_scc1 .LBB5_79
	s_bfe_u32 s5, s4, 0x10006
	s_lshl_b32 s6, s5, 4
	s_mul_i32 s16, s3, 40
	s_mul_hi_i32 s7, s3, 40
	s_add_u32 s22, s0, s16
	s_addc_u32 s23, s1, s7
	s_load_dwordx4 s[16:19], s[22:23], 0x0
	s_load_dwordx2 s[0:1], s[22:23], 0x10
	v_or_b32_e32 v159, s6, v1
	v_lshlrev_b32_e32 v18, 5, v159
	s_waitcnt lgkmcnt(0)
	global_load_dwordx4 v[2:5], v18, s[18:19]
	global_load_dwordx4 v[6:9], v18, s[0:1]
	global_load_dwordx4 v[10:13], v18, s[18:19] offset:16
	global_load_dwordx4 v[14:17], v18, s[0:1] offset:16
	v_bfe_u32 v21, v0, 7, 1
	v_lshrrev_b32_e32 v19, 4, v0
	v_lshlrev_b16_e32 v23, 2, v21
	v_lshrrev_b32_e32 v18, 5, v0
	v_lshrrev_b32_e32 v20, 6, v0
	v_and_b32_e32 v24, 3, v19
	v_bitop3_b16 v19, v23, v19, 3 bitop3:0xf8
	s_movk_i32 s0, 0x3000
	v_and_b32_e32 v18, 4, v18
	v_and_b32_e32 v22, 4, v20
	v_lshlrev_b32_e32 v20, 12, v20
	v_lshlrev_b32_e32 v21, 11, v21
	v_and_b32_e32 v19, 0xffff, v19
	s_bitcmp1_b32 s4, 6
	v_or_b32_e32 v161, v18, v158
	v_and_or_b32 v162, s15, 56, v22
	v_bitop3_b16 v23, v23, 8, v24 bitop3:0xfe
	v_lshlrev_b32_e32 v24, 3, v22
	v_lshl_or_b32 v22, v22, 12, v21
	v_or3_b32 v163, v20, v21, s0
	v_bitop3_b32 v18, v18, v159, v158 bitop3:0x36
	v_bitop3_b32 v19, s6, v19, v1 bitop3:0x36
	s_cselect_b64 s[24:25], -1, 0
	s_and_b32 s0, s15, 0x1ffc0
	s_movk_i32 s1, 0x2000
	v_lshl_or_b32 v168, v18, 4, v22
	v_lshlrev_b32_e32 v18, 4, v19
	v_or_b32_e32 v19, s0, v162
	v_add3_u32 v170, v22, v18, s1
	v_lshl_or_b32 v18, v19, 6, s2
	v_add_u32_e32 v18, v161, v18
	v_mul_u32_u24_e32 v18, 0x600, v18
	v_and_b32_e32 v20, 0xffff, v23
	v_lshl_or_b32 v18, s5, 8, v18
	v_lshlrev_b32_e32 v160, 9, v158
	v_bitop3_b32 v20, s6, v20, v1 bitop3:0x36
	v_lshl_or_b32 v18, v1, 4, v18
	v_add_u32_e32 v164, -1, v162
	v_add_u32_e32 v165, 4, v162
	v_or3_b32 v166, v161, v24, 8
	v_or_b32_e32 v167, 0x1000, v22
	v_lshl_or_b32 v169, v20, 4, v160
	s_and_b32 s17, s17, 0xffff
	s_mov_b32 s19, 0x20000
	s_mov_b32 s18, 0x1800000
	v_add_u32_e32 v171, 0xfffe7c00, v18
	s_mov_b32 s30, s2
	s_waitcnt vmcnt(3)
	v_cvt_pk_f16_f32 v172, v2, v3
	s_waitcnt vmcnt(2)
	v_cvt_pk_f16_f32 v173, v6, v7
	v_cvt_pk_f16_f32 v174, v4, v5
	v_cvt_pk_f16_f32 v175, v8, v9
	s_waitcnt vmcnt(1)
	v_cvt_pk_f16_f32 v176, v10, v11
	s_waitcnt vmcnt(0)
	v_cvt_pk_f16_f32 v177, v14, v15
	v_cvt_pk_f16_f32 v178, v12, v13
	v_cvt_pk_f16_f32 v179, v16, v17
	s_branch .LBB5_4

_Z7k_attn2ILi2EEv8AttnArgs:
	v_readfirstlane_b32 s94, v0
	s_nop 0
	s_lshr_b32 s94, s94, 6
	s_cmp_lt_u32 s94, 4
	s_cbranch_scc1 .Lmyprio6
	s_setprio 1
.Lmyprio6:
	v_readfirstlane_b32 s3, v0
	s_lshl_b32 s12, s3, 1
	v_lshlrev_b32_e32 v3, 3, v0
	s_and_b32 s12, s12, 0x80
	v_and_b32_e32 v3, 0x78, v3
	s_load_dwordx4 s[8:11], s[0:1], 0x0
	s_load_dwordx2 s[4:5], s[0:1], 0x10
	s_load_dwordx2 s[6:7], s[0:1], 0x50
	v_or_b32_e32 v180, s12, v3
	s_lshl_b32 s12, s2, 5
	v_lshrrev_b32_e32 v1, 5, v0
	v_bfe_u32 v2, v0, 4, 2
	s_and_b32 s14, s12, 0xe0
	s_lshr_b32 s12, s2, 3
	v_lshrrev_b32_e32 v0, 6, v0
	v_and_b32_e32 v1, 4, v1
	s_add_i32 s14, s14, s12
	s_and_b32 s2, s2, 56
	v_and_b32_e32 v0, 4, v0
	v_and_or_b32 v181, s14, 56, v0
	v_or3_b32 v182, v2, s2, v1
	s_and_b32 s2, s14, 0x3ffffc0
	v_or_b32_e32 v4, s2, v181
	v_lshlrev_b32_e32 v0, 1, v180
	v_mov_b32_e32 v1, 0
	s_waitcnt lgkmcnt(0)
	v_lshl_add_u64 v[2:3], s[6:7], 0, v[0:1]
	v_lshl_or_b32 v0, v4, 6, v182
	v_lshlrev_b64 v[4:5], 9, v[0:1]
	v_lshl_add_u64 v[8:9], v[2:3], 0, v[4:5]
	v_or_b32_e32 v4, 64, v0
	v_mov_b32_e32 v5, v1
	v_lshlrev_b64 v[4:5], 9, v[4:5]
	v_lshlrev_b32_e32 v20, 2, v180
	v_lshl_add_u64 v[10:11], v[2:3], 0, v[4:5]
	global_load_dwordx4 v[22:25], v20, s[10:11] offset:16
	global_load_dwordx4 v[16:19], v20, s[10:11]
	global_load_dwordx4 v[26:29], v20, s[4:5] offset:16
	global_load_dwordx4 v[30:33], v20, s[4:5]
	global_load_dwordx4 v[12:15], v[8:9], off nt
	global_load_dwordx4 v[4:7], v[10:11], off nt
	v_or_b32_e32 v8, 0x80, v0
	v_mov_b32_e32 v9, v1
	v_lshlrev_b64 v[8:9], 9, v[8:9]
	v_or_b32_e32 v0, 0xc0, v0
	v_lshl_add_u64 v[20:21], v[2:3], 0, v[8:9]
	v_lshlrev_b64 v[0:1], 9, v[0:1]
	v_lshl_add_u64 v[34:35], v[2:3], 0, v[0:1]
	global_load_dwordx4 v[8:11], v[20:21], off nt
	global_load_dwordx4 v[0:3], v[34:35], off nt
	s_bitcmp1_b32 s3, 6
	s_cselect_b64 s[4:5], -1, 0
	s_and_b32 s2, s14, 0x3ffc0
	v_or_b32_e32 v20, s2, v181
	v_lshl_or_b32 v20, v20, 6, v182
	v_add_u32_e32 v184, -1, v182
	v_add_u32_e32 v185, -1, v181
	v_mul_u32_u24_e32 v20, 0x300, v20
	v_or_b32_e32 v34, v185, v184
	v_or_b32_e32 v20, v180, v20
	s_mov_b32 s11, 0x20000
	s_mov_b32 s10, 0x1800000
	s_and_b32 s9, s9, 0xffff
	v_lshlrev_b32_e32 v183, 1, v20
	v_cmp_gt_u32_e64 s[2:3], 64, v34
	s_and_b64 vcc, exec, s[4:5]
	s_waitcnt vmcnt(7)
	v_cvt_pk_f16_f32 v22, v22, v23
	s_waitcnt vmcnt(6)
	v_cvt_pk_f16_f32 v20, v16, v17
	v_cvt_pk_f16_f32 v21, v18, v19
	s_waitcnt vmcnt(4)
	v_cvt_pk_f16_f32 v16, v30, v31
	v_cvt_pk_f16_f32 v17, v32, v33
	v_cvt_pk_f16_f32 v18, v26, v27
	v_cvt_pk_f16_f32 v23, v24, v25
	v_cvt_pk_f16_f32 v19, v28, v29
	s_cbranch_vccz .LBB6_38
	s_load_dwordx2 s[12:13], s[0:1], 0x20
	s_waitcnt lgkmcnt(0)
	s_load_dwordx2 s[4:5], s[12:13], 0x0
	s_load_dword s12, s[12:13], 0x8
	v_cmp_lt_u32_e64 s[64:65], 0, v182
	v_cmp_gt_u32_e64 s[66:67], 63, v182
	v_cmp_lt_u32_e64 s[68:69], 0, v181
	v_cmp_gt_u32_e64 s[70:71], 60, v181
	buffer_load_dwordx4 v[190:193], v183, s[8:11], 0 offen
	s_and_b64 s[72:73], s[68:69], s[64:65]
	s_and_b64 s[74:75], s[68:69], s[66:67]
	s_and_b64 s[76:77], s[70:71], s[64:65]
	s_and_b64 s[78:79], s[70:71], s[66:67]
	v_mov_b32_e32 v136, v20
	v_mov_b32_e32 v137, v21
	v_mov_b32_e32 v138, v22
	v_mov_b32_e32 v139, v23
	v_mov_b32_e32 v96, v16
	v_mov_b32_e32 v97, v17
	v_mov_b32_e32 v98, v18
	v_mov_b32_e32 v99, v19
	v_mov_b32_e32 v152, v20
	v_mov_b32_e32 v153, v21
	v_mov_b32_e32 v154, v22
	v_mov_b32_e32 v155, v23
	v_mov_b32_e32 v124, v16
	v_mov_b32_e32 v125, v17
	v_mov_b32_e32 v126, v18
	v_mov_b32_e32 v127, v19
	v_mov_b32_e32 v160, v20
	v_mov_b32_e32 v161, v21
	v_mov_b32_e32 v162, v22
	v_mov_b32_e32 v163, v23
	v_mov_b32_e32 v140, v16
	v_mov_b32_e32 v141, v17
	v_mov_b32_e32 v142, v18
	v_mov_b32_e32 v143, v19
	v_mov_b32_e32 v112, v20
	v_mov_b32_e32 v113, v21
	v_mov_b32_e32 v114, v22
	v_mov_b32_e32 v115, v23
	v_mov_b32_e32 v68, v16
	v_mov_b32_e32 v69, v17
	v_mov_b32_e32 v70, v18
	v_mov_b32_e32 v71, v19
	v_mov_b32_e32 v148, v20
	v_mov_b32_e32 v149, v21
	v_mov_b32_e32 v150, v22
	v_mov_b32_e32 v151, v23
	v_mov_b32_e32 v108, v16
	v_mov_b32_e32 v109, v17
	v_mov_b32_e32 v110, v18
	v_mov_b32_e32 v111, v19
	v_mov_b32_e32 v76, v20
	v_mov_b32_e32 v77, v21
	v_mov_b32_e32 v78, v22
	v_mov_b32_e32 v79, v23
	v_mov_b32_e32 v48, v16
	v_mov_b32_e32 v49, v17
	v_mov_b32_e32 v50, v18
	v_mov_b32_e32 v51, v19
	v_mov_b32_e32 v116, v20
	v_mov_b32_e32 v117, v21
	v_mov_b32_e32 v118, v22
	v_mov_b32_e32 v119, v23
	v_mov_b32_e32 v72, v16
	v_mov_b32_e32 v73, v17
	v_mov_b32_e32 v74, v18
	v_mov_b32_e32 v75, v19
	v_mov_b32_e32 v44, v20
	v_mov_b32_e32 v45, v21
	v_mov_b32_e32 v46, v22
	v_mov_b32_e32 v47, v23
	v_mov_b32_e32 v32, v16
	v_mov_b32_e32 v33, v17
	v_mov_b32_e32 v34, v18
	v_mov_b32_e32 v35, v19
	v_mov_b32_e32 v80, v20
	v_mov_b32_e32 v81, v21
	v_mov_b32_e32 v82, v22
	v_mov_b32_e32 v83, v23
	v_mov_b32_e32 v40, v16
	v_mov_b32_e32 v41, v17
	v_mov_b32_e32 v42, v18
	v_mov_b32_e32 v43, v19
	v_mov_b32_e32 v100, v20
	v_mov_b32_e32 v101, v21
	v_mov_b32_e32 v102, v22
	v_mov_b32_e32 v103, v23
	v_mov_b32_e32 v52, v16
	v_mov_b32_e32 v53, v17
	v_mov_b32_e32 v54, v18
	v_mov_b32_e32 v55, v19
	v_mov_b32_e32 v144, v20
	v_mov_b32_e32 v145, v21
	v_mov_b32_e32 v146, v22
	v_mov_b32_e32 v147, v23
	v_mov_b32_e32 v84, v16
	v_mov_b32_e32 v85, v17
	v_mov_b32_e32 v86, v18
	v_mov_b32_e32 v87, v19
	v_mov_b32_e32 v156, v20
	v_mov_b32_e32 v157, v21
	v_mov_b32_e32 v158, v22
	v_mov_b32_e32 v159, v23
	v_mov_b32_e32 v104, v16
	v_mov_b32_e32 v105, v17
	v_mov_b32_e32 v106, v18
	v_mov_b32_e32 v107, v19
	v_mov_b32_e32 v164, v20
	v_mov_b32_e32 v165, v21
	v_mov_b32_e32 v166, v22
	v_mov_b32_e32 v167, v23
	v_mov_b32_e32 v120, v16
	v_mov_b32_e32 v121, v17
	v_mov_b32_e32 v122, v18
	v_mov_b32_e32 v123, v19
	v_mov_b32_e32 v28, v20
	v_mov_b32_e32 v29, v21
	v_mov_b32_e32 v30, v22
	v_mov_b32_e32 v31, v23
	v_mov_b32_e32 v24, v16
	v_mov_b32_e32 v25, v17
	v_mov_b32_e32 v26, v18
	v_mov_b32_e32 v27, v19
	v_add_u32_e32 v228, 0xfffe7c00, v183
	v_add_u32_e32 v229, 0xfffe8000, v183
	s_mov_b64 exec, s[72:73]
	buffer_load_dwordx4 v[136:139], v228, s[8:11], 0 offen
	buffer_load_dwordx4 v[96:99], v228, s[8:11], 0 offen offset:512
	s_mov_b64 exec, -1
	s_mov_b64 exec, s[68:69]
	buffer_load_dwordx4 v[152:155], v229, s[8:11], 0 offen offset:512
	buffer_load_dwordx4 v[124:127], v229, s[8:11], 0 offen offset:1024
	s_mov_b64 exec, -1
	s_mov_b64 exec, s[74:75]
	buffer_load_dwordx4 v[160:163], v229, s[8:11], 0 offen offset:2048
	buffer_load_dwordx4 v[140:143], v229, s[8:11], 0 offen offset:2560
	s_mov_b64 exec, -1
	v_add_u32_e32 v228, 0xfffffc00, v183
	s_mov_b64 exec, s[64:65]
	buffer_load_dwordx4 v[112:115], v228, s[8:11], 0 offen
	buffer_load_dwordx4 v[68:71], v228, s[8:11], 0 offen offset:512
	s_mov_b64 exec, -1
	buffer_load_dwordx4 v[132:135], v183, s[8:11], 0 offen offset:512
	buffer_load_dwordx4 v[88:91], v183, s[8:11], 0 offen offset:1024
	s_mov_b64 exec, s[66:67]
	buffer_load_dwordx4 v[148:151], v183, s[8:11], 0 offen offset:2048
	buffer_load_dwordx4 v[108:111], v183, s[8:11], 0 offen offset:2560
	s_mov_b64 exec, -1
	v_add_u32_e32 v228, 0x17c00, v183
	v_add_u32_e32 v229, 0x18000, v183
	s_mov_b64 exec, s[64:65]
	buffer_load_dwordx4 v[76:79], v228, s[8:11], 0 offen
	buffer_load_dwordx4 v[48:51], v228, s[8:11], 0 offen offset:512
	s_mov_b64 exec, -1
	buffer_load_dwordx4 v[92:95], v229, s[8:11], 0 offen offset:512
	buffer_load_dwordx4 v[56:59], v229, s[8:11], 0 offen offset:1024
	s_mov_b64 exec, s[66:67]
	buffer_load_dwordx4 v[116:119], v229, s[8:11], 0 offen offset:2048
	buffer_load_dwordx4 v[72:75], v229, s[8:11], 0 offen offset:2560
	s_mov_b64 exec, -1
	v_add_u32_e32 v228, 0x18000, v183
	buffer_load_dwordx4 v[176:179], v228, s[8:11], 0 offen
	v_add_u32_e32 v229, 0x30000, v183
	buffer_load_dwordx4 v[172:175], v229, s[8:11], 0 offen
	v_add_u32_e32 v228, 0x48000, v183
	buffer_load_dwordx4 v[168:171], v228, s[8:11], 0 offen
	v_add_u32_e32 v228, 0x2fc00, v183
	v_add_u32_e32 v229, 0x30000, v183
	v_add_u32_e32 v230, 0x47c00, v183
	v_add_u32_e32 v231, 0x48000, v183
	v_add_u32_e32 v232, 0x5fc00, v183
	v_add_u32_e32 v233, 0x60000, v183
	s_waitcnt lgkmcnt(0)
	v_cvt_f16_f32_e32 v186, s5
	v_cvt_f16_f32_e32 v188, s4
	v_cvt_f16_f32_e32 v187, s12
	s_waitcnt vmcnt(3)
	v_pk_mul_f16 v196, v188, v193 op_sel_hi:[0,1]
	v_pk_mul_f16 v200, v186, v193 op_sel_hi:[0,1]
	v_pk_mul_f16 v204, v187, v193 op_sel_hi:[0,1]
	v_pk_mul_f16 v189, v188, v190 op_sel_hi:[0,1]
	v_pk_mul_f16 v194, v188, v191 op_sel_hi:[0,1]
	v_pk_mul_f16 v195, v188, v192 op_sel_hi:[0,1]
	v_pk_mul_f16 v197, v186, v190 op_sel_hi:[0,1]
	s_mov_b64 exec, s[64:65]
	buffer_load_dwordx4 v[44:47], v228, s[8:11], 0 offen
	buffer_load_dwordx4 v[32:35], v228, s[8:11], 0 offen offset:512
	s_mov_b64 exec, -1
	v_pk_mul_f16 v198, v186, v191 op_sel_hi:[0,1]
	v_pk_mul_f16 v199, v186, v192 op_sel_hi:[0,1]
	v_pk_mul_f16 v201, v187, v190 op_sel_hi:[0,1]
	v_pk_mul_f16 v202, v187, v191 op_sel_hi:[0,1]
	v_pk_mul_f16 v203, v187, v192 op_sel_hi:[0,1]
	v_pk_fma_f16 v139, v139, v193, v196
	v_pk_fma_f16 v155, v155, v193, v200
	v_pk_fma_f16 v163, v163, v193, v204
	v_pk_fma_f16 v205, v115, v193, v196
	v_pk_fma_f16 v209, v135, v193, v200
	v_pk_fma_f16 v213, v151, v193, v204
	v_pk_fma_f16 v196, v79, v193, v196
	v_pk_fma_f16 v200, v95, v193, v200
	buffer_load_dwordx4 v[60:63], v229, s[8:11], 0 offen offset:512
	buffer_load_dwordx4 v[36:39], v229, s[8:11], 0 offen offset:1024
	v_pk_fma_f16 v193, v119, v193, v204
	v_pk_maximum3_f16 v204, v139, v155, v163
	v_pk_fma_f16 v138, v138, v192, v195
	v_pk_fma_f16 v137, v137, v191, v194
	v_pk_fma_f16 v136, v136, v190, v189
	v_pk_fma_f16 v154, v154, v192, v199
	v_pk_fma_f16 v153, v153, v191, v198
	v_pk_fma_f16 v152, v152, v190, v197
	v_pk_fma_f16 v162, v162, v192, v203
	v_pk_fma_f16 v161, v161, v191, v202
	v_pk_fma_f16 v160, v160, v190, v201
	v_pk_fma_f16 v206, v114, v192, v195
	v_pk_fma_f16 v207, v113, v191, v194
	v_pk_fma_f16 v208, v112, v190, v189
	v_pk_fma_f16 v210, v134, v192, v199
	v_pk_fma_f16 v211, v133, v191, v198
	s_mov_b64 exec, s[66:67]
	buffer_load_dwordx4 v[80:83], v229, s[8:11], 0 offen offset:2048
	buffer_load_dwordx4 v[40:43], v229, s[8:11], 0 offen offset:2560
	s_mov_b64 exec, -1
	v_pk_fma_f16 v212, v132, v190, v197
	v_pk_fma_f16 v214, v150, v192, v203
	v_pk_fma_f16 v215, v149, v191, v202
	v_pk_fma_f16 v216, v148, v190, v201
	v_pk_fma_f16 v195, v78, v192, v195
	v_pk_fma_f16 v194, v77, v191, v194
	v_pk_fma_f16 v189, v76, v190, v189
	v_pk_fma_f16 v199, v94, v192, v199
	v_pk_fma_f16 v198, v93, v191, v198
	v_pk_fma_f16 v197, v92, v190, v197
	v_pk_fma_f16 v192, v118, v192, v203
	v_pk_fma_f16 v191, v117, v191, v202
	v_pk_fma_f16 v190, v116, v190, v201
	v_pk_maximum3_f16 v201, v136, v152, v160
	v_pk_maximum3_f16 v202, v137, v153, v161
	v_pk_maximum3_f16 v203, v138, v154, v162
	v_pk_maximum3_f16 v220, v205, v209, v213
	v_pk_maximum3_f16 v224, v196, v200, v193
	v_pk_maximum3_f16 v217, v208, v212, v216
	v_pk_maximum3_f16 v218, v207, v211, v215
	v_pk_maximum3_f16 v219, v206, v210, v214
	v_pk_maximum3_f16 v221, v189, v197, v190
	v_pk_maximum3_f16 v222, v194, v198, v191
	v_pk_maximum3_f16 v204, v204, v220, v224
	v_pk_maximum3_f16 v223, v195, v199, v192
	v_pk_maximum3_f16 v201, v201, v217, v221
	v_pk_maximum3_f16 v202, v202, v218, v222
	v_pk_maximum3_f16 v203, v203, v219, v223
	v_pk_add_f16 v139, v139, v204 neg_lo:[0,1] neg_hi:[0,1]
	s_mov_b64 exec, s[64:65]
	buffer_load_dwordx4 v[100:103], v230, s[8:11], 0 offen
	buffer_load_dwordx4 v[52:55], v230, s[8:11], 0 offen offset:512
	s_mov_b64 exec, -1
	v_pk_add_f16 v136, v136, v201 neg_lo:[0,1] neg_hi:[0,1]
	v_pk_add_f16 v137, v137, v202 neg_lo:[0,1] neg_hi:[0,1]
	v_pk_add_f16 v138, v138, v203 neg_lo:[0,1] neg_hi:[0,1]
	v_pk_add_f16 v152, v152, v201 neg_lo:[0,1] neg_hi:[0,1]
	v_exp_f16_sdwa v217, v136 dst_sel:WORD_0 dst_unused:UNUSED_PAD src0_sel:WORD_0
	v_exp_f16_sdwa v218, v137 dst_sel:WORD_0 dst_unused:UNUSED_PAD src0_sel:WORD_0
	v_exp_f16_sdwa v219, v138 dst_sel:WORD_0 dst_unused:UNUSED_PAD src0_sel:WORD_0
	v_exp_f16_sdwa v220, v139 dst_sel:WORD_0 dst_unused:UNUSED_PAD src0_sel:WORD_0
	v_exp_f16_sdwa v217, v136 dst_sel:WORD_1 dst_unused:UNUSED_PRESERVE src0_sel:WORD_1
	v_exp_f16_sdwa v218, v137 dst_sel:WORD_1 dst_unused:UNUSED_PRESERVE src0_sel:WORD_1
	v_exp_f16_sdwa v219, v138 dst_sel:WORD_1 dst_unused:UNUSED_PRESERVE src0_sel:WORD_1
	v_exp_f16_sdwa v220, v139 dst_sel:WORD_1 dst_unused:UNUSED_PRESERVE src0_sel:WORD_1
	v_pk_add_f16 v153, v153, v202 neg_lo:[0,1] neg_hi:[0,1]
	v_pk_add_f16 v139, v217, 0
	v_pk_fma_f16 v99, v99, v220, 0
	v_pk_add_f16 v136, v220, 0
	v_pk_add_f16 v137, v219, 0
	v_pk_add_f16 v138, v218, 0
	v_pk_fma_f16 v98, v98, v219, 0
	v_pk_fma_f16 v97, v97, v218, 0
	v_pk_fma_f16 v96, v96, v217, 0
	v_pk_add_f16 v154, v154, v203 neg_lo:[0,1] neg_hi:[0,1]
	buffer_load_dwordx4 v[128:131], v231, s[8:11], 0 offen offset:512
	buffer_load_dwordx4 v[64:67], v231, s[8:11], 0 offen offset:1024
	v_pk_add_f16 v155, v155, v204 neg_lo:[0,1] neg_hi:[0,1]
	v_exp_f16_sdwa v217, v152 dst_sel:WORD_0 dst_unused:UNUSED_PAD src0_sel:WORD_0
	v_exp_f16_sdwa v218, v153 dst_sel:WORD_0 dst_unused:UNUSED_PAD src0_sel:WORD_0
	v_exp_f16_sdwa v219, v154 dst_sel:WORD_0 dst_unused:UNUSED_PAD src0_sel:WORD_0
	v_exp_f16_sdwa v220, v155 dst_sel:WORD_0 dst_unused:UNUSED_PAD src0_sel:WORD_0
	v_exp_f16_sdwa v217, v152 dst_sel:WORD_1 dst_unused:UNUSED_PRESERVE src0_sel:WORD_1
	v_exp_f16_sdwa v218, v153 dst_sel:WORD_1 dst_unused:UNUSED_PRESERVE src0_sel:WORD_1
	v_exp_f16_sdwa v219, v154 dst_sel:WORD_1 dst_unused:UNUSED_PRESERVE src0_sel:WORD_1
	v_exp_f16_sdwa v220, v155 dst_sel:WORD_1 dst_unused:UNUSED_PRESERVE src0_sel:WORD_1
	v_pk_add_f16 v139, v139, v217
	v_pk_fma_f16 v99, v127, v220, v99
	v_pk_add_f16 v127, v163, v204 neg_lo:[0,1] neg_hi:[0,1]
	v_pk_add_f16 v138, v138, v218
	v_pk_add_f16 v137, v137, v219
	v_pk_add_f16 v136, v136, v220
	v_pk_fma_f16 v96, v124, v217, v96
	v_pk_fma_f16 v97, v125, v218, v97
	v_pk_fma_f16 v98, v126, v219, v98
	v_pk_add_f16 v124, v160, v201 neg_lo:[0,1] neg_hi:[0,1]
	v_pk_add_f16 v125, v161, v202 neg_lo:[0,1] neg_hi:[0,1]
	v_pk_add_f16 v126, v162, v203 neg_lo:[0,1] neg_hi:[0,1]
	v_exp_f16_sdwa v152, v124 dst_sel:WORD_0 dst_unused:UNUSED_PAD src0_sel:WORD_0
	v_exp_f16_sdwa v153, v125 dst_sel:WORD_0 dst_unused:UNUSED_PAD src0_sel:WORD_0
	v_exp_f16_sdwa v154, v126 dst_sel:WORD_0 dst_unused:UNUSED_PAD src0_sel:WORD_0
	v_exp_f16_sdwa v155, v127 dst_sel:WORD_0 dst_unused:UNUSED_PAD src0_sel:WORD_0
	v_exp_f16_sdwa v152, v124 dst_sel:WORD_1 dst_unused:UNUSED_PRESERVE src0_sel:WORD_1
	v_exp_f16_sdwa v153, v125 dst_sel:WORD_1 dst_unused:UNUSED_PRESERVE src0_sel:WORD_1
	v_exp_f16_sdwa v154, v126 dst_sel:WORD_1 dst_unused:UNUSED_PRESERVE src0_sel:WORD_1
	v_exp_f16_sdwa v155, v127 dst_sel:WORD_1 dst_unused:UNUSED_PRESERVE src0_sel:WORD_1
	v_pk_add_f16 v127, v139, v152
	v_pk_add_f16 v124, v136, v155
	s_mov_b64 exec, s[66:67]
	buffer_load_dwordx4 v[144:147], v231, s[8:11], 0 offen offset:2048
	buffer_load_dwordx4 v[84:87], v231, s[8:11], 0 offen offset:2560
	s_mov_b64 exec, -1
	v_pk_add_f16 v125, v137, v154
	v_pk_add_f16 v126, v138, v153
	v_pk_fma_f16 v99, v143, v155, v99
	v_pk_fma_f16 v98, v142, v154, v98
	v_pk_fma_f16 v97, v141, v153, v97
	v_pk_fma_f16 v96, v140, v152, v96
	v_pk_add_f16 v136, v208, v201 neg_lo:[0,1] neg_hi:[0,1]
	v_pk_add_f16 v137, v207, v202 neg_lo:[0,1] neg_hi:[0,1]
	v_pk_add_f16 v138, v206, v203 neg_lo:[0,1] neg_hi:[0,1]
	v_pk_add_f16 v139, v205, v204 neg_lo:[0,1] neg_hi:[0,1]
	v_exp_f16_sdwa v140, v136 dst_sel:WORD_0 dst_unused:UNUSED_PAD src0_sel:WORD_0
	v_exp_f16_sdwa v141, v137 dst_sel:WORD_0 dst_unused:UNUSED_PAD src0_sel:WORD_0
	v_exp_f16_sdwa v142, v138 dst_sel:WORD_0 dst_unused:UNUSED_PAD src0_sel:WORD_0
	v_exp_f16_sdwa v143, v139 dst_sel:WORD_0 dst_unused:UNUSED_PAD src0_sel:WORD_0
	v_exp_f16_sdwa v140, v136 dst_sel:WORD_1 dst_unused:UNUSED_PRESERVE src0_sel:WORD_1
	v_exp_f16_sdwa v141, v137 dst_sel:WORD_1 dst_unused:UNUSED_PRESERVE src0_sel:WORD_1
	v_exp_f16_sdwa v142, v138 dst_sel:WORD_1 dst_unused:UNUSED_PRESERVE src0_sel:WORD_1
	v_exp_f16_sdwa v143, v139 dst_sel:WORD_1 dst_unused:UNUSED_PRESERVE src0_sel:WORD_1
	v_pk_add_f16 v136, v212, v201 neg_lo:[0,1] neg_hi:[0,1]
	v_pk_add_f16 v127, v127, v140
	v_pk_add_f16 v126, v126, v141
	v_pk_add_f16 v125, v125, v142
	s_mov_b64 exec, s[76:77]
	buffer_load_dwordx4 v[156:159], v232, s[8:11], 0 offen
	buffer_load_dwordx4 v[104:107], v232, s[8:11], 0 offen offset:512
	s_mov_b64 exec, -1
	v_pk_add_f16 v124, v124, v143
	v_pk_fma_f16 v96, v68, v140, v96
	v_pk_fma_f16 v97, v69, v141, v97
	v_pk_fma_f16 v98, v70, v142, v98
	v_pk_fma_f16 v99, v71, v143, v99
	v_pk_add_f16 v137, v211, v202 neg_lo:[0,1] neg_hi:[0,1]
	v_pk_add_f16 v138, v210, v203 neg_lo:[0,1] neg_hi:[0,1]
	v_pk_add_f16 v139, v209, v204 neg_lo:[0,1] neg_hi:[0,1]
	v_exp_f16_sdwa v140, v136 dst_sel:WORD_0 dst_unused:UNUSED_PAD src0_sel:WORD_0
	v_exp_f16_sdwa v141, v137 dst_sel:WORD_0 dst_unused:UNUSED_PAD src0_sel:WORD_0
	v_exp_f16_sdwa v142, v138 dst_sel:WORD_0 dst_unused:UNUSED_PAD src0_sel:WORD_0
	v_exp_f16_sdwa v143, v139 dst_sel:WORD_0 dst_unused:UNUSED_PAD src0_sel:WORD_0
	v_exp_f16_sdwa v140, v136 dst_sel:WORD_1 dst_unused:UNUSED_PRESERVE src0_sel:WORD_1
	v_exp_f16_sdwa v141, v137 dst_sel:WORD_1 dst_unused:UNUSED_PRESERVE src0_sel:WORD_1
	v_exp_f16_sdwa v142, v138 dst_sel:WORD_1 dst_unused:UNUSED_PRESERVE src0_sel:WORD_1
	v_exp_f16_sdwa v143, v139 dst_sel:WORD_1 dst_unused:UNUSED_PRESERVE src0_sel:WORD_1
	v_pk_add_f16 v136, v216, v201 neg_lo:[0,1] neg_hi:[0,1]
	v_pk_add_f16 v127, v127, v140
	v_pk_add_f16 v124, v124, v143
	v_pk_add_f16 v125, v125, v142
	v_pk_add_f16 v126, v126, v141
	v_pk_fma_f16 v99, v91, v143, v99
	v_pk_fma_f16 v98, v90, v142, v98
	s_mov_b64 exec, s[70:71]
	buffer_load_dwordx4 v[164:167], v233, s[8:11], 0 offen offset:512
	buffer_load_dwordx4 v[120:123], v233, s[8:11], 0 offen offset:1024
	s_mov_b64 exec, -1
	v_pk_fma_f16 v97, v89, v141, v97
	v_pk_fma_f16 v96, v88, v140, v96
	v_pk_add_f16 v137, v215, v202 neg_lo:[0,1] neg_hi:[0,1]
	v_pk_add_f16 v138, v214, v203 neg_lo:[0,1] neg_hi:[0,1]
	v_pk_add_f16 v139, v213, v204 neg_lo:[0,1] neg_hi:[0,1]
	v_exp_f16_sdwa v140, v136 dst_sel:WORD_0 dst_unused:UNUSED_PAD src0_sel:WORD_0
	v_exp_f16_sdwa v141, v137 dst_sel:WORD_0 dst_unused:UNUSED_PAD src0_sel:WORD_0
	v_exp_f16_sdwa v142, v138 dst_sel:WORD_0 dst_unused:UNUSED_PAD src0_sel:WORD_0
	v_exp_f16_sdwa v143, v139 dst_sel:WORD_0 dst_unused:UNUSED_PAD src0_sel:WORD_0
	v_exp_f16_sdwa v140, v136 dst_sel:WORD_1 dst_unused:UNUSED_PRESERVE src0_sel:WORD_1
	v_exp_f16_sdwa v141, v137 dst_sel:WORD_1 dst_unused:UNUSED_PRESERVE src0_sel:WORD_1
	v_exp_f16_sdwa v142, v138 dst_sel:WORD_1 dst_unused:UNUSED_PRESERVE src0_sel:WORD_1
	v_exp_f16_sdwa v143, v139 dst_sel:WORD_1 dst_unused:UNUSED_PRESERVE src0_sel:WORD_1
	v_pk_add_f16 v136, v189, v201 neg_lo:[0,1] neg_hi:[0,1]
	v_pk_add_f16 v127, v127, v140
	v_pk_add_f16 v126, v126, v141
	v_pk_add_f16 v125, v125, v142
	v_pk_add_f16 v124, v124, v143
	v_pk_fma_f16 v96, v108, v140, v96
	v_pk_fma_f16 v97, v109, v141, v97
	v_pk_fma_f16 v98, v110, v142, v98
	v_pk_fma_f16 v99, v111, v143, v99
	s_mov_b64 exec, s[78:79]
	buffer_load_dwordx4 v[28:31], v233, s[8:11], 0 offen offset:2048
	buffer_load_dwordx4 v[24:27], v233, s[8:11], 0 offen offset:2560
	s_mov_b64 exec, -1
	v_pk_add_f16 v137, v194, v202 neg_lo:[0,1] neg_hi:[0,1]
	v_pk_add_f16 v138, v195, v203 neg_lo:[0,1] neg_hi:[0,1]
	v_pk_add_f16 v139, v196, v204 neg_lo:[0,1] neg_hi:[0,1]
	v_exp_f16_sdwa v140, v136 dst_sel:WORD_0 dst_unused:UNUSED_PAD src0_sel:WORD_0
	v_exp_f16_sdwa v141, v137 dst_sel:WORD_0 dst_unused:UNUSED_PAD src0_sel:WORD_0
	v_exp_f16_sdwa v142, v138 dst_sel:WORD_0 dst_unused:UNUSED_PAD src0_sel:WORD_0
	v_exp_f16_sdwa v143, v139 dst_sel:WORD_0 dst_unused:UNUSED_PAD src0_sel:WORD_0
	v_exp_f16_sdwa v140, v136 dst_sel:WORD_1 dst_unused:UNUSED_PRESERVE src0_sel:WORD_1
	v_exp_f16_sdwa v141, v137 dst_sel:WORD_1 dst_unused:UNUSED_PRESERVE src0_sel:WORD_1
	v_exp_f16_sdwa v142, v138 dst_sel:WORD_1 dst_unused:UNUSED_PRESERVE src0_sel:WORD_1
	v_exp_f16_sdwa v143, v139 dst_sel:WORD_1 dst_unused:UNUSED_PRESERVE src0_sel:WORD_1
	v_pk_add_f16 v136, v197, v201 neg_lo:[0,1] neg_hi:[0,1]
	v_pk_add_f16 v127, v127, v140
	v_pk_add_f16 v124, v124, v143
	v_pk_add_f16 v125, v125, v142
	v_pk_add_f16 v126, v126, v141
	v_pk_fma_f16 v99, v51, v143, v99
	v_pk_fma_f16 v98, v50, v142, v98
	v_pk_fma_f16 v97, v49, v141, v97
	v_pk_fma_f16 v96, v48, v140, v96
	v_pk_add_f16 v137, v198, v202 neg_lo:[0,1] neg_hi:[0,1]
	v_pk_add_f16 v138, v199, v203 neg_lo:[0,1] neg_hi:[0,1]
	v_pk_add_f16 v139, v200, v204 neg_lo:[0,1] neg_hi:[0,1]
	v_exp_f16_sdwa v140, v136 dst_sel:WORD_0 dst_unused:UNUSED_PAD src0_sel:WORD_0
	v_exp_f16_sdwa v141, v137 dst_sel:WORD_0 dst_unused:UNUSED_PAD src0_sel:WORD_0
	v_exp_f16_sdwa v142, v138 dst_sel:WORD_0 dst_unused:UNUSED_PAD src0_sel:WORD_0
	v_exp_f16_sdwa v143, v139 dst_sel:WORD_0 dst_unused:UNUSED_PAD src0_sel:WORD_0
	v_exp_f16_sdwa v140, v136 dst_sel:WORD_1 dst_unused:UNUSED_PRESERVE src0_sel:WORD_1
	v_exp_f16_sdwa v141, v137 dst_sel:WORD_1 dst_unused:UNUSED_PRESERVE src0_sel:WORD_1
	v_exp_f16_sdwa v142, v138 dst_sel:WORD_1 dst_unused:UNUSED_PRESERVE src0_sel:WORD_1
	v_exp_f16_sdwa v143, v139 dst_sel:WORD_1 dst_unused:UNUSED_PRESERVE src0_sel:WORD_1
	v_pk_add_f16 v136, v190, v201 neg_lo:[0,1] neg_hi:[0,1]
	v_pk_add_f16 v127, v127, v140
	v_pk_add_f16 v126, v126, v141
	v_pk_add_f16 v125, v125, v142
	v_pk_add_f16 v124, v124, v143
	v_pk_fma_f16 v96, v56, v140, v96
	v_pk_fma_f16 v97, v57, v141, v97
	v_pk_fma_f16 v98, v58, v142, v98
	v_pk_fma_f16 v99, v59, v143, v99
	v_pk_add_f16 v137, v191, v202 neg_lo:[0,1] neg_hi:[0,1]
	v_pk_add_f16 v138, v192, v203 neg_lo:[0,1] neg_hi:[0,1]
	v_pk_add_f16 v139, v193, v204 neg_lo:[0,1] neg_hi:[0,1]
	v_exp_f16_sdwa v140, v136 dst_sel:WORD_0 dst_unused:UNUSED_PAD src0_sel:WORD_0
	v_exp_f16_sdwa v141, v137 dst_sel:WORD_0 dst_unused:UNUSED_PAD src0_sel:WORD_0
	v_exp_f16_sdwa v142, v138 dst_sel:WORD_0 dst_unused:UNUSED_PAD src0_sel:WORD_0
	v_exp_f16_sdwa v143, v139 dst_sel:WORD_0 dst_unused:UNUSED_PAD src0_sel:WORD_0
	v_exp_f16_sdwa v140, v136 dst_sel:WORD_1 dst_unused:UNUSED_PRESERVE src0_sel:WORD_1
	v_exp_f16_sdwa v141, v137 dst_sel:WORD_1 dst_unused:UNUSED_PRESERVE src0_sel:WORD_1
	v_exp_f16_sdwa v142, v138 dst_sel:WORD_1 dst_unused:UNUSED_PRESERVE src0_sel:WORD_1
	v_exp_f16_sdwa v143, v139 dst_sel:WORD_1 dst_unused:UNUSED_PRESERVE src0_sel:WORD_1
	v_pk_add_f16 v127, v127, v140
	v_pk_add_f16 v126, v126, v141
	v_rcp_f16_e32 v136, v127
	v_rcp_f16_sdwa v127, v127 dst_sel:DWORD dst_unused:UNUSED_PAD src0_sel:WORD_1
	v_pk_add_f16 v125, v125, v142
	v_rcp_f16_e32 v137, v126
	v_rcp_f16_sdwa v126, v126 dst_sel:DWORD dst_unused:UNUSED_PAD src0_sel:WORD_1
	v_pk_add_f16 v124, v124, v143
	v_rcp_f16_e32 v138, v125
	v_rcp_f16_sdwa v139, v125 dst_sel:DWORD dst_unused:UNUSED_PAD src0_sel:WORD_1
	v_pk_fma_f16 v97, v73, v141, v97
	v_pk_fma_f16 v96, v72, v140, v96
	v_rcp_f16_e32 v140, v124
	v_rcp_f16_sdwa v141, v124 dst_sel:DWORD dst_unused:UNUSED_PAD src0_sel:WORD_1
	v_pack_b32_f16 v124, v136, v127
	v_pk_mul_f16 v124, v96, v124
	v_pack_b32_f16 v96, v137, v126
	v_pk_fma_f16 v98, v74, v142, v98
	v_pk_mul_f16 v125, v97, v96
	v_pack_b32_f16 v96, v138, v139
	v_pk_fma_f16 v99, v75, v143, v99
	v_pk_mul_f16 v126, v98, v96
	v_pack_b32_f16 v96, v140, v141
	v_pk_mul_f16 v127, v99, v96
	s_waitcnt vmcnt(12)
	v_pk_mul_f16 v99, v188, v179 op_sel_hi:[0,1]
	v_pk_mul_f16 v139, v186, v179 op_sel_hi:[0,1]
	v_pk_mul_f16 v143, v187, v179 op_sel_hi:[0,1]
	v_pk_mul_f16 v96, v188, v176 op_sel_hi:[0,1]
	v_pk_mul_f16 v97, v188, v177 op_sel_hi:[0,1]
	v_pk_mul_f16 v98, v188, v178 op_sel_hi:[0,1]
	v_pk_mul_f16 v136, v186, v176 op_sel_hi:[0,1]
	v_pk_mul_f16 v137, v186, v177 op_sel_hi:[0,1]
	v_pk_mul_f16 v138, v186, v178 op_sel_hi:[0,1]
	v_pk_mul_f16 v140, v187, v176 op_sel_hi:[0,1]
	v_pk_mul_f16 v141, v187, v177 op_sel_hi:[0,1]
	v_pk_mul_f16 v142, v187, v178 op_sel_hi:[0,1]
	v_pk_fma_f16 v115, v115, v179, v99
	v_pk_fma_f16 v135, v135, v179, v139
	v_pk_fma_f16 v151, v151, v179, v143
	v_pk_fma_f16 v152, v79, v179, v99
	v_pk_fma_f16 v160, v95, v179, v139
	v_pk_fma_f16 v189, v119, v179, v143
	v_pk_fma_f16 v99, v47, v179, v99
	v_pk_fma_f16 v139, v63, v179, v139
	v_pk_fma_f16 v143, v83, v179, v143
	v_pk_maximum3_f16 v179, v115, v135, v151
	v_pk_fma_f16 v114, v114, v178, v98
	v_pk_fma_f16 v113, v113, v177, v97
	v_pk_fma_f16 v112, v112, v176, v96
	v_pk_fma_f16 v134, v134, v178, v138
	v_pk_fma_f16 v133, v133, v177, v137
	v_pk_fma_f16 v132, v132, v176, v136
	v_pk_fma_f16 v150, v150, v178, v142
	v_pk_fma_f16 v149, v149, v177, v141
	v_pk_fma_f16 v148, v148, v176, v140
	v_pk_fma_f16 v153, v78, v178, v98
	v_pk_fma_f16 v154, v77, v177, v97
	v_pk_fma_f16 v155, v76, v176, v96
	v_pk_fma_f16 v161, v94, v178, v138
	v_pk_fma_f16 v162, v93, v177, v137
	v_pk_fma_f16 v163, v92, v176, v136
	v_pk_fma_f16 v190, v118, v178, v142
	v_pk_fma_f16 v191, v117, v177, v141
	v_pk_fma_f16 v192, v116, v176, v140
	v_pk_fma_f16 v98, v46, v178, v98
	v_pk_fma_f16 v97, v45, v177, v97
	v_pk_fma_f16 v96, v44, v176, v96
	v_pk_fma_f16 v138, v62, v178, v138
	v_pk_fma_f16 v137, v61, v177, v137
	v_pk_fma_f16 v136, v60, v176, v136
	v_pk_fma_f16 v142, v82, v178, v142
	v_pk_fma_f16 v141, v81, v177, v141
	v_pk_fma_f16 v140, v80, v176, v140
	v_pk_maximum3_f16 v176, v112, v132, v148
	v_pk_maximum3_f16 v177, v113, v133, v149
	v_pk_maximum3_f16 v178, v114, v134, v150
	v_pk_maximum3_f16 v196, v152, v160, v189
	v_pk_maximum3_f16 v200, v99, v139, v143
	v_pk_maximum3_f16 v193, v155, v163, v192
	v_pk_maximum3_f16 v194, v154, v162, v191
	v_pk_maximum3_f16 v195, v153, v161, v190
	v_pk_maximum3_f16 v197, v96, v136, v140
	v_pk_maximum3_f16 v198, v97, v137, v141
	v_pk_maximum3_f16 v179, v179, v196, v200
	v_pk_maximum3_f16 v199, v98, v138, v142
	v_pk_maximum3_f16 v176, v176, v193, v197
	v_pk_maximum3_f16 v177, v177, v194, v198
	v_pk_maximum3_f16 v178, v178, v195, v199
	v_pk_add_f16 v115, v115, v179 neg_lo:[0,1] neg_hi:[0,1]
	v_pk_add_f16 v112, v112, v176 neg_lo:[0,1] neg_hi:[0,1]
	v_pk_add_f16 v113, v113, v177 neg_lo:[0,1] neg_hi:[0,1]
	v_pk_add_f16 v114, v114, v178 neg_lo:[0,1] neg_hi:[0,1]
	v_pk_add_f16 v132, v132, v176 neg_lo:[0,1] neg_hi:[0,1]
	v_exp_f16_sdwa v193, v112 dst_sel:WORD_0 dst_unused:UNUSED_PAD src0_sel:WORD_0
	v_exp_f16_sdwa v194, v113 dst_sel:WORD_0 dst_unused:UNUSED_PAD src0_sel:WORD_0
	v_exp_f16_sdwa v195, v114 dst_sel:WORD_0 dst_unused:UNUSED_PAD src0_sel:WORD_0
	v_exp_f16_sdwa v196, v115 dst_sel:WORD_0 dst_unused:UNUSED_PAD src0_sel:WORD_0
	v_exp_f16_sdwa v193, v112 dst_sel:WORD_1 dst_unused:UNUSED_PRESERVE src0_sel:WORD_1
	v_exp_f16_sdwa v194, v113 dst_sel:WORD_1 dst_unused:UNUSED_PRESERVE src0_sel:WORD_1
	v_exp_f16_sdwa v195, v114 dst_sel:WORD_1 dst_unused:UNUSED_PRESERVE src0_sel:WORD_1
	v_exp_f16_sdwa v196, v115 dst_sel:WORD_1 dst_unused:UNUSED_PRESERVE src0_sel:WORD_1
	v_pk_add_f16 v133, v133, v177 neg_lo:[0,1] neg_hi:[0,1]
	v_pk_add_f16 v115, v193, 0
	v_pk_fma_f16 v71, v71, v196, 0
	v_pk_add_f16 v112, v196, 0
	v_pk_add_f16 v113, v195, 0
	v_pk_add_f16 v114, v194, 0
	v_pk_fma_f16 v70, v70, v195, 0
	v_pk_fma_f16 v69, v69, v194, 0
	v_pk_fma_f16 v68, v68, v193, 0
	v_pk_add_f16 v134, v134, v178 neg_lo:[0,1] neg_hi:[0,1]
	v_pk_add_f16 v135, v135, v179 neg_lo:[0,1] neg_hi:[0,1]
	v_pk_add_f16 v96, v96, v176 neg_lo:[0,1] neg_hi:[0,1]
	v_exp_f16_sdwa v193, v132 dst_sel:WORD_0 dst_unused:UNUSED_PAD src0_sel:WORD_0
	v_exp_f16_sdwa v194, v133 dst_sel:WORD_0 dst_unused:UNUSED_PAD src0_sel:WORD_0
	v_exp_f16_sdwa v195, v134 dst_sel:WORD_0 dst_unused:UNUSED_PAD src0_sel:WORD_0
	v_exp_f16_sdwa v196, v135 dst_sel:WORD_0 dst_unused:UNUSED_PAD src0_sel:WORD_0
	v_exp_f16_sdwa v193, v132 dst_sel:WORD_1 dst_unused:UNUSED_PRESERVE src0_sel:WORD_1
	v_exp_f16_sdwa v194, v133 dst_sel:WORD_1 dst_unused:UNUSED_PRESERVE src0_sel:WORD_1
	v_exp_f16_sdwa v195, v134 dst_sel:WORD_1 dst_unused:UNUSED_PRESERVE src0_sel:WORD_1
	v_exp_f16_sdwa v196, v135 dst_sel:WORD_1 dst_unused:UNUSED_PRESERVE src0_sel:WORD_1
	v_pk_add_f16 v97, v97, v177 neg_lo:[0,1] neg_hi:[0,1]
	v_pk_add_f16 v115, v115, v193
	v_pk_fma_f16 v71, v91, v196, v71
	v_pk_add_f16 v91, v151, v179 neg_lo:[0,1] neg_hi:[0,1]
	v_pk_add_f16 v114, v114, v194
	v_pk_add_f16 v113, v113, v195
	v_pk_add_f16 v112, v112, v196
	v_pk_fma_f16 v68, v88, v193, v68
	v_pk_fma_f16 v69, v89, v194, v69
	v_pk_fma_f16 v70, v90, v195, v70
	v_pk_add_f16 v88, v148, v176 neg_lo:[0,1] neg_hi:[0,1]
	v_pk_add_f16 v89, v149, v177 neg_lo:[0,1] neg_hi:[0,1]
	v_pk_add_f16 v90, v150, v178 neg_lo:[0,1] neg_hi:[0,1]
	v_pk_add_f16 v98, v98, v178 neg_lo:[0,1] neg_hi:[0,1]
	v_exp_f16_sdwa v132, v88 dst_sel:WORD_0 dst_unused:UNUSED_PAD src0_sel:WORD_0
	v_exp_f16_sdwa v133, v89 dst_sel:WORD_0 dst_unused:UNUSED_PAD src0_sel:WORD_0
	v_exp_f16_sdwa v134, v90 dst_sel:WORD_0 dst_unused:UNUSED_PAD src0_sel:WORD_0
	v_exp_f16_sdwa v135, v91 dst_sel:WORD_0 dst_unused:UNUSED_PAD src0_sel:WORD_0
	v_exp_f16_sdwa v132, v88 dst_sel:WORD_1 dst_unused:UNUSED_PRESERVE src0_sel:WORD_1
	v_exp_f16_sdwa v133, v89 dst_sel:WORD_1 dst_unused:UNUSED_PRESERVE src0_sel:WORD_1
	v_exp_f16_sdwa v134, v90 dst_sel:WORD_1 dst_unused:UNUSED_PRESERVE src0_sel:WORD_1
	v_exp_f16_sdwa v135, v91 dst_sel:WORD_1 dst_unused:UNUSED_PRESERVE src0_sel:WORD_1
	v_pk_add_f16 v99, v99, v179 neg_lo:[0,1] neg_hi:[0,1]
	v_pk_add_f16 v91, v115, v132
	v_pk_add_f16 v88, v112, v135
	v_pk_add_f16 v89, v113, v134
	v_pk_add_f16 v90, v114, v133
	v_pk_fma_f16 v71, v111, v135, v71
	v_pk_fma_f16 v70, v110, v134, v70
	v_pk_fma_f16 v69, v109, v133, v69
	v_pk_fma_f16 v68, v108, v132, v68
	v_pk_add_f16 v108, v155, v176 neg_lo:[0,1] neg_hi:[0,1]
	v_pk_add_f16 v109, v154, v177 neg_lo:[0,1] neg_hi:[0,1]
	v_pk_add_f16 v110, v153, v178 neg_lo:[0,1] neg_hi:[0,1]
	v_pk_add_f16 v111, v152, v179 neg_lo:[0,1] neg_hi:[0,1]
	v_exp_f16_sdwa v112, v108 dst_sel:WORD_0 dst_unused:UNUSED_PAD src0_sel:WORD_0
	v_exp_f16_sdwa v113, v109 dst_sel:WORD_0 dst_unused:UNUSED_PAD src0_sel:WORD_0
	v_exp_f16_sdwa v114, v110 dst_sel:WORD_0 dst_unused:UNUSED_PAD src0_sel:WORD_0
	v_exp_f16_sdwa v115, v111 dst_sel:WORD_0 dst_unused:UNUSED_PAD src0_sel:WORD_0
	v_exp_f16_sdwa v112, v108 dst_sel:WORD_1 dst_unused:UNUSED_PRESERVE src0_sel:WORD_1
	v_exp_f16_sdwa v113, v109 dst_sel:WORD_1 dst_unused:UNUSED_PRESERVE src0_sel:WORD_1
	v_exp_f16_sdwa v114, v110 dst_sel:WORD_1 dst_unused:UNUSED_PRESERVE src0_sel:WORD_1
	v_exp_f16_sdwa v115, v111 dst_sel:WORD_1 dst_unused:UNUSED_PRESERVE src0_sel:WORD_1
	v_pk_add_f16 v108, v163, v176 neg_lo:[0,1] neg_hi:[0,1]
	v_pk_add_f16 v91, v91, v112
	v_pk_add_f16 v90, v90, v113
	v_pk_add_f16 v89, v89, v114
	v_pk_add_f16 v88, v88, v115
	v_pk_fma_f16 v68, v48, v112, v68
	v_pk_fma_f16 v69, v49, v113, v69
	v_pk_fma_f16 v70, v50, v114, v70
	v_pk_fma_f16 v71, v51, v115, v71
	v_pk_add_f16 v109, v162, v177 neg_lo:[0,1] neg_hi:[0,1]
	v_pk_add_f16 v110, v161, v178 neg_lo:[0,1] neg_hi:[0,1]
	v_pk_add_f16 v111, v160, v179 neg_lo:[0,1] neg_hi:[0,1]
	v_exp_f16_sdwa v112, v108 dst_sel:WORD_0 dst_unused:UNUSED_PAD src0_sel:WORD_0
	v_exp_f16_sdwa v113, v109 dst_sel:WORD_0 dst_unused:UNUSED_PAD src0_sel:WORD_0
	v_exp_f16_sdwa v114, v110 dst_sel:WORD_0 dst_unused:UNUSED_PAD src0_sel:WORD_0
	v_exp_f16_sdwa v115, v111 dst_sel:WORD_0 dst_unused:UNUSED_PAD src0_sel:WORD_0
	v_exp_f16_sdwa v112, v108 dst_sel:WORD_1 dst_unused:UNUSED_PRESERVE src0_sel:WORD_1
	v_exp_f16_sdwa v113, v109 dst_sel:WORD_1 dst_unused:UNUSED_PRESERVE src0_sel:WORD_1
	v_exp_f16_sdwa v114, v110 dst_sel:WORD_1 dst_unused:UNUSED_PRESERVE src0_sel:WORD_1
	v_exp_f16_sdwa v115, v111 dst_sel:WORD_1 dst_unused:UNUSED_PRESERVE src0_sel:WORD_1
	v_pk_add_f16 v108, v192, v176 neg_lo:[0,1] neg_hi:[0,1]
	v_pk_add_f16 v91, v91, v112
	v_pk_add_f16 v88, v88, v115
	v_pk_add_f16 v89, v89, v114
	v_pk_add_f16 v90, v90, v113
	v_pk_fma_f16 v71, v59, v115, v71
	v_pk_fma_f16 v70, v58, v114, v70
	v_pk_fma_f16 v69, v57, v113, v69
	v_pk_fma_f16 v68, v56, v112, v68
	v_pk_add_f16 v109, v191, v177 neg_lo:[0,1] neg_hi:[0,1]
	v_pk_add_f16 v110, v190, v178 neg_lo:[0,1] neg_hi:[0,1]
	v_pk_add_f16 v111, v189, v179 neg_lo:[0,1] neg_hi:[0,1]
	v_exp_f16_sdwa v112, v108 dst_sel:WORD_0 dst_unused:UNUSED_PAD src0_sel:WORD_0
	v_exp_f16_sdwa v113, v109 dst_sel:WORD_0 dst_unused:UNUSED_PAD src0_sel:WORD_0
	v_exp_f16_sdwa v114, v110 dst_sel:WORD_0 dst_unused:UNUSED_PAD src0_sel:WORD_0
	v_exp_f16_sdwa v115, v111 dst_sel:WORD_0 dst_unused:UNUSED_PAD src0_sel:WORD_0
	v_exp_f16_sdwa v112, v108 dst_sel:WORD_1 dst_unused:UNUSED_PRESERVE src0_sel:WORD_1
	v_exp_f16_sdwa v113, v109 dst_sel:WORD_1 dst_unused:UNUSED_PRESERVE src0_sel:WORD_1
	v_exp_f16_sdwa v114, v110 dst_sel:WORD_1 dst_unused:UNUSED_PRESERVE src0_sel:WORD_1
	v_exp_f16_sdwa v115, v111 dst_sel:WORD_1 dst_unused:UNUSED_PRESERVE src0_sel:WORD_1
	v_exp_f16_sdwa v108, v96 dst_sel:WORD_0 dst_unused:UNUSED_PAD src0_sel:WORD_0
	v_exp_f16_sdwa v109, v97 dst_sel:WORD_0 dst_unused:UNUSED_PAD src0_sel:WORD_0
	v_exp_f16_sdwa v110, v98 dst_sel:WORD_0 dst_unused:UNUSED_PAD src0_sel:WORD_0
	v_exp_f16_sdwa v111, v99 dst_sel:WORD_0 dst_unused:UNUSED_PAD src0_sel:WORD_0
	v_exp_f16_sdwa v108, v96 dst_sel:WORD_1 dst_unused:UNUSED_PRESERVE src0_sel:WORD_1
	v_exp_f16_sdwa v109, v97 dst_sel:WORD_1 dst_unused:UNUSED_PRESERVE src0_sel:WORD_1
	v_exp_f16_sdwa v110, v98 dst_sel:WORD_1 dst_unused:UNUSED_PRESERVE src0_sel:WORD_1
	v_exp_f16_sdwa v111, v99 dst_sel:WORD_1 dst_unused:UNUSED_PRESERVE src0_sel:WORD_1
	v_pk_add_f16 v96, v136, v176 neg_lo:[0,1] neg_hi:[0,1]
	v_pk_add_f16 v91, v91, v112
	v_pk_add_f16 v90, v90, v113
	v_pk_add_f16 v89, v89, v114
	v_pk_add_f16 v88, v88, v115
	v_pk_fma_f16 v68, v72, v112, v68
	v_pk_fma_f16 v69, v73, v113, v69
	v_pk_fma_f16 v70, v74, v114, v70
	v_pk_fma_f16 v71, v75, v115, v71
	v_pk_add_f16 v91, v91, v108
	v_pk_add_f16 v88, v88, v111
	v_pk_add_f16 v89, v89, v110
	v_pk_add_f16 v90, v90, v109
	v_pk_fma_f16 v71, v35, v111, v71
	v_pk_fma_f16 v70, v34, v110, v70
	v_pk_fma_f16 v69, v33, v109, v69
	v_pk_fma_f16 v68, v32, v108, v68
	v_pk_add_f16 v97, v137, v177 neg_lo:[0,1] neg_hi:[0,1]
	v_pk_add_f16 v98, v138, v178 neg_lo:[0,1] neg_hi:[0,1]
	v_pk_add_f16 v99, v139, v179 neg_lo:[0,1] neg_hi:[0,1]
	v_exp_f16_sdwa v108, v96 dst_sel:WORD_0 dst_unused:UNUSED_PAD src0_sel:WORD_0
	v_exp_f16_sdwa v109, v97 dst_sel:WORD_0 dst_unused:UNUSED_PAD src0_sel:WORD_0
	v_exp_f16_sdwa v110, v98 dst_sel:WORD_0 dst_unused:UNUSED_PAD src0_sel:WORD_0
	v_exp_f16_sdwa v111, v99 dst_sel:WORD_0 dst_unused:UNUSED_PAD src0_sel:WORD_0
	v_exp_f16_sdwa v108, v96 dst_sel:WORD_1 dst_unused:UNUSED_PRESERVE src0_sel:WORD_1
	v_exp_f16_sdwa v109, v97 dst_sel:WORD_1 dst_unused:UNUSED_PRESERVE src0_sel:WORD_1
	v_exp_f16_sdwa v110, v98 dst_sel:WORD_1 dst_unused:UNUSED_PRESERVE src0_sel:WORD_1
	v_exp_f16_sdwa v111, v99 dst_sel:WORD_1 dst_unused:UNUSED_PRESERVE src0_sel:WORD_1
	v_pk_add_f16 v96, v140, v176 neg_lo:[0,1] neg_hi:[0,1]
	v_pk_add_f16 v91, v91, v108
	v_pk_add_f16 v90, v90, v109
	v_pk_add_f16 v89, v89, v110
	v_pk_add_f16 v88, v88, v111
	v_pk_fma_f16 v68, v36, v108, v68
	v_pk_fma_f16 v69, v37, v109, v69
	v_pk_fma_f16 v70, v38, v110, v70
	v_pk_fma_f16 v71, v39, v111, v71
	v_pk_add_f16 v97, v141, v177 neg_lo:[0,1] neg_hi:[0,1]
	v_pk_add_f16 v98, v142, v178 neg_lo:[0,1] neg_hi:[0,1]
	v_pk_add_f16 v99, v143, v179 neg_lo:[0,1] neg_hi:[0,1]
	v_exp_f16_sdwa v108, v96 dst_sel:WORD_0 dst_unused:UNUSED_PAD src0_sel:WORD_0
	v_exp_f16_sdwa v109, v97 dst_sel:WORD_0 dst_unused:UNUSED_PAD src0_sel:WORD_0
	v_exp_f16_sdwa v110, v98 dst_sel:WORD_0 dst_unused:UNUSED_PAD src0_sel:WORD_0
	v_exp_f16_sdwa v111, v99 dst_sel:WORD_0 dst_unused:UNUSED_PAD src0_sel:WORD_0
	v_exp_f16_sdwa v108, v96 dst_sel:WORD_1 dst_unused:UNUSED_PRESERVE src0_sel:WORD_1
	v_exp_f16_sdwa v109, v97 dst_sel:WORD_1 dst_unused:UNUSED_PRESERVE src0_sel:WORD_1
	v_exp_f16_sdwa v110, v98 dst_sel:WORD_1 dst_unused:UNUSED_PRESERVE src0_sel:WORD_1
	v_exp_f16_sdwa v111, v99 dst_sel:WORD_1 dst_unused:UNUSED_PRESERVE src0_sel:WORD_1
	v_pk_add_f16 v91, v91, v108
	v_pk_add_f16 v90, v90, v109
	v_rcp_f16_e32 v96, v91
	v_rcp_f16_sdwa v91, v91 dst_sel:DWORD dst_unused:UNUSED_PAD src0_sel:WORD_1
	v_pk_add_f16 v89, v89, v110
	v_rcp_f16_e32 v97, v90
	v_rcp_f16_sdwa v90, v90 dst_sel:DWORD dst_unused:UNUSED_PAD src0_sel:WORD_1
	v_pk_add_f16 v88, v88, v111
	v_rcp_f16_e32 v98, v89
	v_rcp_f16_sdwa v99, v89 dst_sel:DWORD dst_unused:UNUSED_PAD src0_sel:WORD_1
	v_pk_fma_f16 v69, v41, v109, v69
	v_pk_fma_f16 v68, v40, v108, v68
	v_rcp_f16_e32 v108, v88
	v_rcp_f16_sdwa v109, v88 dst_sel:DWORD dst_unused:UNUSED_PAD src0_sel:WORD_1
	v_pack_b32_f16 v88, v96, v91
	v_pk_mul_f16 v88, v68, v88
	v_pack_b32_f16 v68, v97, v90
	v_pk_fma_f16 v70, v42, v110, v70
	v_pk_mul_f16 v89, v69, v68
	v_pack_b32_f16 v68, v98, v99
	v_pk_fma_f16 v71, v43, v111, v71
	v_pk_mul_f16 v90, v70, v68
	v_pack_b32_f16 v68, v108, v109
	v_pk_mul_f16 v91, v71, v68
	s_waitcnt vmcnt(6)
	v_pk_mul_f16 v68, v188, v172 op_sel_hi:[0,1]
	v_pk_mul_f16 v96, v186, v172 op_sel_hi:[0,1]
	v_pk_mul_f16 v108, v187, v172 op_sel_hi:[0,1]
	v_pk_mul_f16 v69, v188, v173 op_sel_hi:[0,1]
	v_pk_mul_f16 v70, v188, v174 op_sel_hi:[0,1]
	v_pk_mul_f16 v71, v188, v175 op_sel_hi:[0,1]
	v_pk_mul_f16 v97, v186, v173 op_sel_hi:[0,1]
	v_pk_mul_f16 v98, v186, v174 op_sel_hi:[0,1]
	v_pk_mul_f16 v99, v186, v175 op_sel_hi:[0,1]
	v_pk_mul_f16 v109, v187, v173 op_sel_hi:[0,1]
	v_pk_mul_f16 v110, v187, v174 op_sel_hi:[0,1]
	v_pk_mul_f16 v111, v187, v175 op_sel_hi:[0,1]
	v_pk_fma_f16 v76, v76, v172, v68
	v_pk_fma_f16 v92, v92, v172, v96
	v_pk_fma_f16 v115, v116, v172, v108
	v_pk_fma_f16 v79, v79, v175, v71
	v_pk_maximum3_f16 v140, v76, v92, v115
	v_pk_fma_f16 v78, v78, v174, v70
	v_pk_fma_f16 v77, v77, v173, v69
	v_pk_fma_f16 v95, v95, v175, v99
	v_pk_fma_f16 v94, v94, v174, v98
	v_pk_fma_f16 v93, v93, v173, v97
	v_pk_fma_f16 v112, v119, v175, v111
	v_pk_fma_f16 v113, v118, v174, v110
	v_pk_fma_f16 v114, v117, v173, v109
	v_pk_fma_f16 v119, v44, v172, v68
	v_pk_fma_f16 v135, v60, v172, v96
	v_pk_fma_f16 v139, v80, v172, v108
	v_pk_fma_f16 v68, v100, v172, v68
	v_pk_fma_f16 v96, v128, v172, v96
	v_pk_fma_f16 v108, v144, v172, v108
	v_pk_maximum3_f16 v141, v77, v93, v114
	v_pk_maximum3_f16 v142, v78, v94, v113
	v_pk_maximum3_f16 v143, v79, v95, v112
	v_pk_maximum3_f16 v148, v119, v135, v139
	v_pk_fma_f16 v116, v47, v175, v71
	v_pk_maximum3_f16 v152, v68, v96, v108
	v_pk_fma_f16 v117, v46, v174, v70
	v_pk_maximum3_f16 v140, v140, v148, v152
	v_pk_fma_f16 v118, v45, v173, v69
	v_pk_fma_f16 v132, v63, v175, v99
	v_pk_fma_f16 v133, v62, v174, v98
	v_pk_fma_f16 v134, v61, v173, v97
	v_pk_fma_f16 v136, v83, v175, v111
	v_pk_fma_f16 v137, v82, v174, v110
	v_pk_fma_f16 v138, v81, v173, v109
	v_pk_fma_f16 v71, v103, v175, v71
	v_pk_fma_f16 v70, v102, v174, v70
	v_pk_fma_f16 v69, v101, v173, v69
	v_pk_fma_f16 v99, v131, v175, v99
	v_pk_fma_f16 v98, v130, v174, v98
	v_pk_fma_f16 v97, v129, v173, v97
	v_pk_fma_f16 v111, v147, v175, v111
	v_pk_fma_f16 v110, v146, v174, v110
	v_pk_fma_f16 v109, v145, v173, v109
	v_pk_maximum3_f16 v149, v118, v134, v138
	v_pk_maximum3_f16 v150, v117, v133, v137
	v_pk_maximum3_f16 v151, v116, v132, v136
	v_pk_maximum3_f16 v154, v70, v98, v110
	v_pk_maximum3_f16 v155, v71, v99, v111
	v_pk_maximum3_f16 v153, v69, v97, v109
	v_pk_maximum3_f16 v141, v141, v149, v153
	v_pk_maximum3_f16 v142, v142, v150, v154
	v_pk_maximum3_f16 v143, v143, v151, v155
	v_pk_add_f16 v76, v76, v140 neg_lo:[0,1] neg_hi:[0,1]
	v_pk_add_f16 v77, v77, v141 neg_lo:[0,1] neg_hi:[0,1]
	v_pk_add_f16 v78, v78, v142 neg_lo:[0,1] neg_hi:[0,1]
	v_pk_add_f16 v79, v79, v143 neg_lo:[0,1] neg_hi:[0,1]
	v_pk_add_f16 v92, v92, v140 neg_lo:[0,1] neg_hi:[0,1]
	v_exp_f16_sdwa v148, v76 dst_sel:WORD_0 dst_unused:UNUSED_PAD src0_sel:WORD_0
	v_exp_f16_sdwa v149, v77 dst_sel:WORD_0 dst_unused:UNUSED_PAD src0_sel:WORD_0
	v_exp_f16_sdwa v150, v78 dst_sel:WORD_0 dst_unused:UNUSED_PAD src0_sel:WORD_0
	v_exp_f16_sdwa v151, v79 dst_sel:WORD_0 dst_unused:UNUSED_PAD src0_sel:WORD_0
	v_exp_f16_sdwa v148, v76 dst_sel:WORD_1 dst_unused:UNUSED_PRESERVE src0_sel:WORD_1
	v_exp_f16_sdwa v149, v77 dst_sel:WORD_1 dst_unused:UNUSED_PRESERVE src0_sel:WORD_1
	v_exp_f16_sdwa v150, v78 dst_sel:WORD_1 dst_unused:UNUSED_PRESERVE src0_sel:WORD_1
	v_exp_f16_sdwa v151, v79 dst_sel:WORD_1 dst_unused:UNUSED_PRESERVE src0_sel:WORD_1
	v_pk_add_f16 v93, v93, v141 neg_lo:[0,1] neg_hi:[0,1]
	v_pk_add_f16 v76, v151, 0
	v_pk_fma_f16 v48, v48, v148, 0
	v_pk_add_f16 v77, v150, 0
	v_pk_add_f16 v78, v149, 0
	v_pk_add_f16 v79, v148, 0
	v_pk_fma_f16 v49, v49, v149, 0
	v_pk_fma_f16 v50, v50, v150, 0
	v_pk_fma_f16 v51, v51, v151, 0
	v_pk_add_f16 v94, v94, v142 neg_lo:[0,1] neg_hi:[0,1]
	v_pk_add_f16 v95, v95, v143 neg_lo:[0,1] neg_hi:[0,1]
	v_pk_add_f16 v68, v68, v140 neg_lo:[0,1] neg_hi:[0,1]
	v_exp_f16_sdwa v148, v92 dst_sel:WORD_0 dst_unused:UNUSED_PAD src0_sel:WORD_0
	v_exp_f16_sdwa v149, v93 dst_sel:WORD_0 dst_unused:UNUSED_PAD src0_sel:WORD_0
	v_exp_f16_sdwa v150, v94 dst_sel:WORD_0 dst_unused:UNUSED_PAD src0_sel:WORD_0
	v_exp_f16_sdwa v151, v95 dst_sel:WORD_0 dst_unused:UNUSED_PAD src0_sel:WORD_0
	v_exp_f16_sdwa v148, v92 dst_sel:WORD_1 dst_unused:UNUSED_PRESERVE src0_sel:WORD_1
	v_exp_f16_sdwa v149, v93 dst_sel:WORD_1 dst_unused:UNUSED_PRESERVE src0_sel:WORD_1
	v_exp_f16_sdwa v150, v94 dst_sel:WORD_1 dst_unused:UNUSED_PRESERVE src0_sel:WORD_1
	v_exp_f16_sdwa v151, v95 dst_sel:WORD_1 dst_unused:UNUSED_PRESERVE src0_sel:WORD_1
	v_pk_add_f16 v69, v69, v141 neg_lo:[0,1] neg_hi:[0,1]
	v_pk_add_f16 v76, v76, v151
	v_pk_fma_f16 v48, v56, v148, v48
	v_pk_add_f16 v56, v115, v140 neg_lo:[0,1] neg_hi:[0,1]
	v_pk_add_f16 v79, v79, v148
	v_pk_add_f16 v78, v78, v149
	v_pk_add_f16 v77, v77, v150
	v_pk_fma_f16 v51, v59, v151, v51
	v_pk_fma_f16 v50, v58, v150, v50
	v_pk_fma_f16 v49, v57, v149, v49
	v_pk_add_f16 v57, v114, v141 neg_lo:[0,1] neg_hi:[0,1]
	v_pk_add_f16 v58, v113, v142 neg_lo:[0,1] neg_hi:[0,1]
	v_pk_add_f16 v59, v112, v143 neg_lo:[0,1] neg_hi:[0,1]
	v_pk_add_f16 v70, v70, v142 neg_lo:[0,1] neg_hi:[0,1]
	v_exp_f16_sdwa v92, v56 dst_sel:WORD_0 dst_unused:UNUSED_PAD src0_sel:WORD_0
	v_exp_f16_sdwa v93, v57 dst_sel:WORD_0 dst_unused:UNUSED_PAD src0_sel:WORD_0
	v_exp_f16_sdwa v94, v58 dst_sel:WORD_0 dst_unused:UNUSED_PAD src0_sel:WORD_0
	v_exp_f16_sdwa v95, v59 dst_sel:WORD_0 dst_unused:UNUSED_PAD src0_sel:WORD_0
	v_exp_f16_sdwa v92, v56 dst_sel:WORD_1 dst_unused:UNUSED_PRESERVE src0_sel:WORD_1
	v_exp_f16_sdwa v93, v57 dst_sel:WORD_1 dst_unused:UNUSED_PRESERVE src0_sel:WORD_1
	v_exp_f16_sdwa v94, v58 dst_sel:WORD_1 dst_unused:UNUSED_PRESERVE src0_sel:WORD_1
	v_exp_f16_sdwa v95, v59 dst_sel:WORD_1 dst_unused:UNUSED_PRESERVE src0_sel:WORD_1
	v_pk_add_f16 v71, v71, v143 neg_lo:[0,1] neg_hi:[0,1]
	v_pk_add_f16 v56, v76, v95
	v_pk_add_f16 v57, v77, v94
	v_pk_add_f16 v58, v78, v93
	v_pk_add_f16 v59, v79, v92
	v_pk_fma_f16 v48, v72, v92, v48
	v_pk_fma_f16 v49, v73, v93, v49
	v_pk_fma_f16 v50, v74, v94, v50
	v_pk_fma_f16 v51, v75, v95, v51
	v_pk_add_f16 v72, v119, v140 neg_lo:[0,1] neg_hi:[0,1]
	v_pk_add_f16 v73, v118, v141 neg_lo:[0,1] neg_hi:[0,1]
	v_pk_add_f16 v74, v117, v142 neg_lo:[0,1] neg_hi:[0,1]
	v_pk_add_f16 v75, v116, v143 neg_lo:[0,1] neg_hi:[0,1]
	v_exp_f16_sdwa v76, v72 dst_sel:WORD_0 dst_unused:UNUSED_PAD src0_sel:WORD_0
	v_exp_f16_sdwa v77, v73 dst_sel:WORD_0 dst_unused:UNUSED_PAD src0_sel:WORD_0
	v_exp_f16_sdwa v78, v74 dst_sel:WORD_0 dst_unused:UNUSED_PAD src0_sel:WORD_0
	v_exp_f16_sdwa v79, v75 dst_sel:WORD_0 dst_unused:UNUSED_PAD src0_sel:WORD_0
	v_exp_f16_sdwa v76, v72 dst_sel:WORD_1 dst_unused:UNUSED_PRESERVE src0_sel:WORD_1
	v_exp_f16_sdwa v77, v73 dst_sel:WORD_1 dst_unused:UNUSED_PRESERVE src0_sel:WORD_1
	v_exp_f16_sdwa v78, v74 dst_sel:WORD_1 dst_unused:UNUSED_PRESERVE src0_sel:WORD_1
	v_exp_f16_sdwa v79, v75 dst_sel:WORD_1 dst_unused:UNUSED_PRESERVE src0_sel:WORD_1
	v_pk_add_f16 v72, v135, v140 neg_lo:[0,1] neg_hi:[0,1]
	v_pk_add_f16 v56, v56, v79
	v_pk_add_f16 v59, v59, v76
	v_pk_add_f16 v58, v58, v77
	v_pk_add_f16 v57, v57, v78
	v_pk_fma_f16 v51, v35, v79, v51
	v_pk_fma_f16 v50, v34, v78, v50
	v_pk_fma_f16 v49, v33, v77, v49
	v_pk_fma_f16 v48, v32, v76, v48
	v_pk_add_f16 v73, v134, v141 neg_lo:[0,1] neg_hi:[0,1]
	v_pk_add_f16 v74, v133, v142 neg_lo:[0,1] neg_hi:[0,1]
	v_pk_add_f16 v75, v132, v143 neg_lo:[0,1] neg_hi:[0,1]
	v_exp_f16_sdwa v76, v72 dst_sel:WORD_0 dst_unused:UNUSED_PAD src0_sel:WORD_0
	v_exp_f16_sdwa v77, v73 dst_sel:WORD_0 dst_unused:UNUSED_PAD src0_sel:WORD_0
	v_exp_f16_sdwa v78, v74 dst_sel:WORD_0 dst_unused:UNUSED_PAD src0_sel:WORD_0
	v_exp_f16_sdwa v79, v75 dst_sel:WORD_0 dst_unused:UNUSED_PAD src0_sel:WORD_0
	v_exp_f16_sdwa v76, v72 dst_sel:WORD_1 dst_unused:UNUSED_PRESERVE src0_sel:WORD_1
	v_exp_f16_sdwa v77, v73 dst_sel:WORD_1 dst_unused:UNUSED_PRESERVE src0_sel:WORD_1
	v_exp_f16_sdwa v78, v74 dst_sel:WORD_1 dst_unused:UNUSED_PRESERVE src0_sel:WORD_1
	v_exp_f16_sdwa v79, v75 dst_sel:WORD_1 dst_unused:UNUSED_PRESERVE src0_sel:WORD_1
	v_pk_add_f16 v72, v139, v140 neg_lo:[0,1] neg_hi:[0,1]
	v_pk_add_f16 v56, v56, v79
	v_pk_add_f16 v57, v57, v78
	v_pk_add_f16 v58, v58, v77
	v_pk_add_f16 v59, v59, v76
	v_pk_fma_f16 v48, v36, v76, v48
	v_pk_fma_f16 v49, v37, v77, v49
	v_pk_fma_f16 v50, v38, v78, v50
	v_pk_fma_f16 v51, v39, v79, v51
	v_pk_add_f16 v73, v138, v141 neg_lo:[0,1] neg_hi:[0,1]
	v_pk_add_f16 v74, v137, v142 neg_lo:[0,1] neg_hi:[0,1]
	v_pk_add_f16 v75, v136, v143 neg_lo:[0,1] neg_hi:[0,1]
	v_exp_f16_sdwa v76, v72 dst_sel:WORD_0 dst_unused:UNUSED_PAD src0_sel:WORD_0
	v_exp_f16_sdwa v77, v73 dst_sel:WORD_0 dst_unused:UNUSED_PAD src0_sel:WORD_0
	v_exp_f16_sdwa v78, v74 dst_sel:WORD_0 dst_unused:UNUSED_PAD src0_sel:WORD_0
	v_exp_f16_sdwa v79, v75 dst_sel:WORD_0 dst_unused:UNUSED_PAD src0_sel:WORD_0
	v_exp_f16_sdwa v76, v72 dst_sel:WORD_1 dst_unused:UNUSED_PRESERVE src0_sel:WORD_1
	v_exp_f16_sdwa v77, v73 dst_sel:WORD_1 dst_unused:UNUSED_PRESERVE src0_sel:WORD_1
	v_exp_f16_sdwa v78, v74 dst_sel:WORD_1 dst_unused:UNUSED_PRESERVE src0_sel:WORD_1
	v_exp_f16_sdwa v79, v75 dst_sel:WORD_1 dst_unused:UNUSED_PRESERVE src0_sel:WORD_1
	v_exp_f16_sdwa v72, v68 dst_sel:WORD_0 dst_unused:UNUSED_PAD src0_sel:WORD_0
	v_exp_f16_sdwa v73, v69 dst_sel:WORD_0 dst_unused:UNUSED_PAD src0_sel:WORD_0
	v_exp_f16_sdwa v74, v70 dst_sel:WORD_0 dst_unused:UNUSED_PAD src0_sel:WORD_0
	v_exp_f16_sdwa v75, v71 dst_sel:WORD_0 dst_unused:UNUSED_PAD src0_sel:WORD_0
	v_exp_f16_sdwa v72, v68 dst_sel:WORD_1 dst_unused:UNUSED_PRESERVE src0_sel:WORD_1
	v_exp_f16_sdwa v73, v69 dst_sel:WORD_1 dst_unused:UNUSED_PRESERVE src0_sel:WORD_1
	v_exp_f16_sdwa v74, v70 dst_sel:WORD_1 dst_unused:UNUSED_PRESERVE src0_sel:WORD_1
	v_exp_f16_sdwa v75, v71 dst_sel:WORD_1 dst_unused:UNUSED_PRESERVE src0_sel:WORD_1
	v_pk_add_f16 v68, v96, v140 neg_lo:[0,1] neg_hi:[0,1]
	v_pk_add_f16 v56, v56, v79
	v_pk_add_f16 v59, v59, v76
	v_pk_add_f16 v58, v58, v77
	v_pk_add_f16 v57, v57, v78
	v_pk_fma_f16 v51, v43, v79, v51
	v_pk_fma_f16 v50, v42, v78, v50
	v_pk_fma_f16 v49, v41, v77, v49
	v_pk_fma_f16 v48, v40, v76, v48
	v_pk_add_f16 v56, v56, v75
	v_pk_add_f16 v57, v57, v74
	v_pk_add_f16 v58, v58, v73
	v_pk_add_f16 v59, v59, v72
	v_pk_fma_f16 v48, v52, v72, v48
	v_pk_fma_f16 v49, v53, v73, v49
	v_pk_fma_f16 v50, v54, v74, v50
	v_pk_fma_f16 v51, v55, v75, v51
	v_pk_add_f16 v69, v97, v141 neg_lo:[0,1] neg_hi:[0,1]
	v_pk_add_f16 v70, v98, v142 neg_lo:[0,1] neg_hi:[0,1]
	v_pk_add_f16 v71, v99, v143 neg_lo:[0,1] neg_hi:[0,1]
	v_exp_f16_sdwa v72, v68 dst_sel:WORD_0 dst_unused:UNUSED_PAD src0_sel:WORD_0
	v_exp_f16_sdwa v73, v69 dst_sel:WORD_0 dst_unused:UNUSED_PAD src0_sel:WORD_0
	v_exp_f16_sdwa v74, v70 dst_sel:WORD_0 dst_unused:UNUSED_PAD src0_sel:WORD_0
	v_exp_f16_sdwa v75, v71 dst_sel:WORD_0 dst_unused:UNUSED_PAD src0_sel:WORD_0
	v_exp_f16_sdwa v72, v68 dst_sel:WORD_1 dst_unused:UNUSED_PRESERVE src0_sel:WORD_1
	v_exp_f16_sdwa v73, v69 dst_sel:WORD_1 dst_unused:UNUSED_PRESERVE src0_sel:WORD_1
	v_exp_f16_sdwa v74, v70 dst_sel:WORD_1 dst_unused:UNUSED_PRESERVE src0_sel:WORD_1
	v_exp_f16_sdwa v75, v71 dst_sel:WORD_1 dst_unused:UNUSED_PRESERVE src0_sel:WORD_1
	v_pk_add_f16 v68, v108, v140 neg_lo:[0,1] neg_hi:[0,1]
	v_pk_add_f16 v56, v56, v75
	v_pk_add_f16 v59, v59, v72
	v_pk_add_f16 v58, v58, v73
	v_pk_add_f16 v57, v57, v74
	v_pk_fma_f16 v51, v67, v75, v51
	v_pk_fma_f16 v50, v66, v74, v50
	v_pk_fma_f16 v49, v65, v73, v49
	v_pk_fma_f16 v48, v64, v72, v48
	v_pk_add_f16 v69, v109, v141 neg_lo:[0,1] neg_hi:[0,1]
	v_pk_add_f16 v70, v110, v142 neg_lo:[0,1] neg_hi:[0,1]
	v_pk_add_f16 v71, v111, v143 neg_lo:[0,1] neg_hi:[0,1]
	v_exp_f16_sdwa v72, v68 dst_sel:WORD_0 dst_unused:UNUSED_PAD src0_sel:WORD_0
	v_exp_f16_sdwa v73, v69 dst_sel:WORD_0 dst_unused:UNUSED_PAD src0_sel:WORD_0
	v_exp_f16_sdwa v74, v70 dst_sel:WORD_0 dst_unused:UNUSED_PAD src0_sel:WORD_0
	v_exp_f16_sdwa v75, v71 dst_sel:WORD_0 dst_unused:UNUSED_PAD src0_sel:WORD_0
	v_exp_f16_sdwa v72, v68 dst_sel:WORD_1 dst_unused:UNUSED_PRESERVE src0_sel:WORD_1
	v_exp_f16_sdwa v73, v69 dst_sel:WORD_1 dst_unused:UNUSED_PRESERVE src0_sel:WORD_1
	v_exp_f16_sdwa v74, v70 dst_sel:WORD_1 dst_unused:UNUSED_PRESERVE src0_sel:WORD_1
	v_exp_f16_sdwa v75, v71 dst_sel:WORD_1 dst_unused:UNUSED_PRESERVE src0_sel:WORD_1
	s_nop 0
	v_pk_add_f16 v56, v56, v75
	v_pk_add_f16 v57, v57, v74
	v_rcp_f16_e32 v70, v56
	v_rcp_f16_sdwa v56, v56 dst_sel:DWORD dst_unused:UNUSED_PAD src0_sel:WORD_1
	v_pk_add_f16 v58, v58, v73
	v_rcp_f16_e32 v71, v57
	v_rcp_f16_sdwa v57, v57 dst_sel:DWORD dst_unused:UNUSED_PAD src0_sel:WORD_1
	v_pk_add_f16 v59, v59, v72
	v_rcp_f16_e32 v69, v58
	v_rcp_f16_sdwa v58, v58 dst_sel:DWORD dst_unused:UNUSED_PAD src0_sel:WORD_1
	v_rcp_f16_e32 v68, v59
	v_rcp_f16_sdwa v59, v59 dst_sel:DWORD dst_unused:UNUSED_PAD src0_sel:WORD_1
	v_pk_fma_f16 v51, v87, v75, v51
	v_pack_b32_f16 v56, v70, v56
	v_pk_fma_f16 v50, v86, v74, v50
	v_pk_mul_f16 v51, v51, v56
	v_pack_b32_f16 v56, v71, v57
	v_pk_fma_f16 v49, v85, v73, v49
	v_pk_mul_f16 v50, v50, v56
	v_pack_b32_f16 v56, v69, v58
	v_pk_fma_f16 v48, v84, v72, v48
	v_pk_mul_f16 v49, v49, v56
	v_pack_b32_f16 v56, v68, v59
	v_pk_mul_f16 v48, v48, v56
	s_waitcnt vmcnt(0)
	v_pk_mul_f16 v56, v188, v168 op_sel_hi:[0,1]
	v_pk_mul_f16 v57, v188, v169 op_sel_hi:[0,1]
	v_pk_mul_f16 v58, v188, v170 op_sel_hi:[0,1]
	v_pk_mul_f16 v59, v188, v171 op_sel_hi:[0,1]
	v_pk_mul_f16 v68, v186, v168 op_sel_hi:[0,1]
	v_pk_mul_f16 v69, v186, v169 op_sel_hi:[0,1]
	v_pk_mul_f16 v70, v186, v170 op_sel_hi:[0,1]
	v_pk_mul_f16 v71, v186, v171 op_sel_hi:[0,1]
	v_pk_mul_f16 v72, v187, v168 op_sel_hi:[0,1]
	v_pk_mul_f16 v73, v187, v169 op_sel_hi:[0,1]
	v_pk_mul_f16 v74, v187, v170 op_sel_hi:[0,1]
	v_pk_mul_f16 v75, v187, v171 op_sel_hi:[0,1]
	v_pk_fma_f16 v47, v47, v171, v59
	v_pk_fma_f16 v46, v46, v170, v58
	v_pk_fma_f16 v45, v45, v169, v57
	v_pk_fma_f16 v44, v44, v168, v56
	v_pk_fma_f16 v63, v63, v171, v71
	v_pk_fma_f16 v62, v62, v170, v70
	v_pk_fma_f16 v61, v61, v169, v69
	v_pk_fma_f16 v60, v60, v168, v68
	v_pk_fma_f16 v76, v83, v171, v75
	v_pk_fma_f16 v77, v82, v170, v74
	v_pk_fma_f16 v78, v81, v169, v73
	v_pk_fma_f16 v79, v80, v168, v72
	v_pk_fma_f16 v80, v103, v171, v59
	v_pk_fma_f16 v81, v102, v170, v58
	v_pk_fma_f16 v82, v101, v169, v57
	v_pk_fma_f16 v83, v100, v168, v56
	v_pk_fma_f16 v92, v131, v171, v71
	v_pk_fma_f16 v93, v130, v170, v70
	v_pk_fma_f16 v94, v129, v169, v69
	v_pk_fma_f16 v95, v128, v168, v68
	v_pk_fma_f16 v96, v147, v171, v75
	v_pk_fma_f16 v97, v146, v170, v74
	v_pk_fma_f16 v98, v145, v169, v73
	v_pk_fma_f16 v99, v144, v168, v72
	v_pk_fma_f16 v75, v31, v171, v75
	v_pk_fma_f16 v74, v30, v170, v74
	v_pk_fma_f16 v73, v29, v169, v73
	v_pk_fma_f16 v72, v28, v168, v72
	v_pk_maximum3_f16 v28, v44, v60, v79
	v_pk_maximum3_f16 v29, v45, v61, v78
	v_pk_maximum3_f16 v30, v46, v62, v77
	v_pk_maximum3_f16 v31, v47, v63, v76
	v_pk_maximum3_f16 v100, v83, v95, v99
	v_pk_maximum3_f16 v101, v82, v94, v98
	v_pk_maximum3_f16 v102, v81, v93, v97
	v_pk_maximum3_f16 v103, v80, v92, v96
	v_pk_fma_f16 v59, v159, v171, v59
	v_pk_fma_f16 v58, v158, v170, v58
	v_pk_fma_f16 v57, v157, v169, v57
	v_pk_fma_f16 v56, v156, v168, v56
	v_pk_fma_f16 v71, v167, v171, v71
	v_pk_fma_f16 v70, v166, v170, v70
	v_pk_fma_f16 v69, v165, v169, v69
	v_pk_fma_f16 v68, v164, v168, v68
	v_pk_maximum3_f16 v109, v57, v69, v73
	v_pk_maximum3_f16 v110, v58, v70, v74
	v_pk_maximum3_f16 v111, v59, v71, v75
	v_pk_maximum3_f16 v108, v56, v68, v72
	v_pk_maximum3_f16 v29, v29, v101, v109
	v_pk_maximum3_f16 v30, v30, v102, v110
	v_pk_maximum3_f16 v31, v31, v103, v111
	v_pk_maximum3_f16 v28, v28, v100, v108
	v_xor_b32_e32 v100, 0x80008000, v31
	v_xor_b32_e32 v101, 0x80008000, v30
	v_xor_b32_e32 v102, 0x80008000, v29
	v_xor_b32_e32 v103, 0x80008000, v28
	v_pk_add_f16 v28, v44, v103
	v_pk_add_f16 v29, v45, v102
	v_pk_add_f16 v30, v46, v101
	v_pk_add_f16 v31, v47, v100
	v_exp_f16_sdwa v44, v28 dst_sel:WORD_0 dst_unused:UNUSED_PAD src0_sel:WORD_0
	v_exp_f16_sdwa v45, v29 dst_sel:WORD_0 dst_unused:UNUSED_PAD src0_sel:WORD_0
	v_exp_f16_sdwa v46, v30 dst_sel:WORD_0 dst_unused:UNUSED_PAD src0_sel:WORD_0
	v_exp_f16_sdwa v47, v31 dst_sel:WORD_0 dst_unused:UNUSED_PAD src0_sel:WORD_0
	v_exp_f16_sdwa v44, v28 dst_sel:WORD_1 dst_unused:UNUSED_PRESERVE src0_sel:WORD_1
	v_exp_f16_sdwa v45, v29 dst_sel:WORD_1 dst_unused:UNUSED_PRESERVE src0_sel:WORD_1
	v_exp_f16_sdwa v46, v30 dst_sel:WORD_1 dst_unused:UNUSED_PRESERVE src0_sel:WORD_1
	v_exp_f16_sdwa v47, v31 dst_sel:WORD_1 dst_unused:UNUSED_PRESERVE src0_sel:WORD_1
	v_pk_add_f16 v28, v44, 0
	v_pk_add_f16 v29, v45, 0
	v_pk_add_f16 v30, v46, 0
	v_pk_add_f16 v31, v47, 0
	v_pk_fma_f16 v32, v32, v44, 0
	v_pk_fma_f16 v33, v33, v45, 0
	v_pk_fma_f16 v34, v34, v46, 0
	v_pk_fma_f16 v35, v35, v47, 0
	v_pk_add_f16 v44, v60, v103
	v_pk_add_f16 v45, v61, v102
	v_pk_add_f16 v46, v62, v101
	v_pk_add_f16 v47, v63, v100
	v_exp_f16_sdwa v60, v44 dst_sel:WORD_0 dst_unused:UNUSED_PAD src0_sel:WORD_0
	v_exp_f16_sdwa v61, v45 dst_sel:WORD_0 dst_unused:UNUSED_PAD src0_sel:WORD_0
	v_exp_f16_sdwa v62, v46 dst_sel:WORD_0 dst_unused:UNUSED_PAD src0_sel:WORD_0
	v_exp_f16_sdwa v63, v47 dst_sel:WORD_0 dst_unused:UNUSED_PAD src0_sel:WORD_0
	v_exp_f16_sdwa v60, v44 dst_sel:WORD_1 dst_unused:UNUSED_PRESERVE src0_sel:WORD_1
	v_exp_f16_sdwa v61, v45 dst_sel:WORD_1 dst_unused:UNUSED_PRESERVE src0_sel:WORD_1
	v_exp_f16_sdwa v62, v46 dst_sel:WORD_1 dst_unused:UNUSED_PRESERVE src0_sel:WORD_1
	v_exp_f16_sdwa v63, v47 dst_sel:WORD_1 dst_unused:UNUSED_PRESERVE src0_sel:WORD_1
	s_nop 0
	v_pk_add_f16 v31, v31, v63
	v_pk_add_f16 v30, v30, v62
	v_pk_add_f16 v29, v29, v61
	v_pk_add_f16 v28, v28, v60
	v_pk_fma_f16 v35, v39, v63, v35
	v_pk_fma_f16 v34, v38, v62, v34
	v_pk_fma_f16 v33, v37, v61, v33
	v_pk_fma_f16 v32, v36, v60, v32
	v_pk_add_f16 v36, v79, v103
	v_pk_add_f16 v37, v78, v102
	v_pk_add_f16 v38, v77, v101
	v_pk_add_f16 v39, v76, v100
	v_exp_f16_sdwa v44, v36 dst_sel:WORD_0 dst_unused:UNUSED_PAD src0_sel:WORD_0
	v_exp_f16_sdwa v45, v37 dst_sel:WORD_0 dst_unused:UNUSED_PAD src0_sel:WORD_0
	v_exp_f16_sdwa v46, v38 dst_sel:WORD_0 dst_unused:UNUSED_PAD src0_sel:WORD_0
	v_exp_f16_sdwa v47, v39 dst_sel:WORD_0 dst_unused:UNUSED_PAD src0_sel:WORD_0
	v_exp_f16_sdwa v44, v36 dst_sel:WORD_1 dst_unused:UNUSED_PRESERVE src0_sel:WORD_1
	v_exp_f16_sdwa v45, v37 dst_sel:WORD_1 dst_unused:UNUSED_PRESERVE src0_sel:WORD_1
	v_exp_f16_sdwa v46, v38 dst_sel:WORD_1 dst_unused:UNUSED_PRESERVE src0_sel:WORD_1
	v_exp_f16_sdwa v47, v39 dst_sel:WORD_1 dst_unused:UNUSED_PRESERVE src0_sel:WORD_1
	v_pk_add_f16 v36, v83, v103
	v_pk_add_f16 v28, v28, v44
	v_pk_add_f16 v29, v29, v45
	v_pk_add_f16 v30, v30, v46
	v_pk_add_f16 v31, v31, v47
	v_pk_fma_f16 v32, v40, v44, v32
	v_pk_fma_f16 v33, v41, v45, v33
	v_pk_fma_f16 v34, v42, v46, v34
	v_pk_fma_f16 v35, v43, v47, v35
	v_pk_add_f16 v37, v82, v102
	v_pk_add_f16 v38, v81, v101
	v_pk_add_f16 v39, v80, v100
	v_exp_f16_sdwa v40, v36 dst_sel:WORD_0 dst_unused:UNUSED_PAD src0_sel:WORD_0
	v_exp_f16_sdwa v41, v37 dst_sel:WORD_0 dst_unused:UNUSED_PAD src0_sel:WORD_0
	v_exp_f16_sdwa v42, v38 dst_sel:WORD_0 dst_unused:UNUSED_PAD src0_sel:WORD_0
	v_exp_f16_sdwa v43, v39 dst_sel:WORD_0 dst_unused:UNUSED_PAD src0_sel:WORD_0
	v_exp_f16_sdwa v40, v36 dst_sel:WORD_1 dst_unused:UNUSED_PRESERVE src0_sel:WORD_1
	v_exp_f16_sdwa v41, v37 dst_sel:WORD_1 dst_unused:UNUSED_PRESERVE src0_sel:WORD_1
	v_exp_f16_sdwa v42, v38 dst_sel:WORD_1 dst_unused:UNUSED_PRESERVE src0_sel:WORD_1
	v_exp_f16_sdwa v43, v39 dst_sel:WORD_1 dst_unused:UNUSED_PRESERVE src0_sel:WORD_1
	v_pk_add_f16 v36, v95, v103
	v_pk_add_f16 v31, v31, v43
	v_pk_add_f16 v30, v30, v42
	v_pk_add_f16 v29, v29, v41
	v_pk_add_f16 v28, v28, v40
	v_pk_fma_f16 v35, v55, v43, v35
	v_pk_fma_f16 v34, v54, v42, v34
	v_pk_fma_f16 v33, v53, v41, v33
	v_pk_fma_f16 v32, v52, v40, v32
	v_pk_add_f16 v37, v94, v102
	v_pk_add_f16 v38, v93, v101
	v_pk_add_f16 v39, v92, v100
	v_exp_f16_sdwa v40, v36 dst_sel:WORD_0 dst_unused:UNUSED_PAD src0_sel:WORD_0
	v_exp_f16_sdwa v41, v37 dst_sel:WORD_0 dst_unused:UNUSED_PAD src0_sel:WORD_0
	v_exp_f16_sdwa v42, v38 dst_sel:WORD_0 dst_unused:UNUSED_PAD src0_sel:WORD_0
	v_exp_f16_sdwa v43, v39 dst_sel:WORD_0 dst_unused:UNUSED_PAD src0_sel:WORD_0
	v_exp_f16_sdwa v40, v36 dst_sel:WORD_1 dst_unused:UNUSED_PRESERVE src0_sel:WORD_1
	v_exp_f16_sdwa v41, v37 dst_sel:WORD_1 dst_unused:UNUSED_PRESERVE src0_sel:WORD_1
	v_exp_f16_sdwa v42, v38 dst_sel:WORD_1 dst_unused:UNUSED_PRESERVE src0_sel:WORD_1
	v_exp_f16_sdwa v43, v39 dst_sel:WORD_1 dst_unused:UNUSED_PRESERVE src0_sel:WORD_1
	v_pk_add_f16 v36, v99, v103
	v_pk_add_f16 v28, v28, v40
	v_pk_add_f16 v29, v29, v41
	v_pk_add_f16 v30, v30, v42
	v_pk_add_f16 v31, v31, v43
	v_pk_fma_f16 v32, v64, v40, v32
	v_pk_fma_f16 v33, v65, v41, v33
	v_pk_fma_f16 v34, v66, v42, v34
	v_pk_fma_f16 v35, v67, v43, v35
	v_pk_add_f16 v37, v98, v102
	v_pk_add_f16 v38, v97, v101
	v_pk_add_f16 v39, v96, v100
	v_exp_f16_sdwa v40, v36 dst_sel:WORD_0 dst_unused:UNUSED_PAD src0_sel:WORD_0
	v_exp_f16_sdwa v41, v37 dst_sel:WORD_0 dst_unused:UNUSED_PAD src0_sel:WORD_0
	v_exp_f16_sdwa v42, v38 dst_sel:WORD_0 dst_unused:UNUSED_PAD src0_sel:WORD_0
	v_exp_f16_sdwa v43, v39 dst_sel:WORD_0 dst_unused:UNUSED_PAD src0_sel:WORD_0
	v_exp_f16_sdwa v40, v36 dst_sel:WORD_1 dst_unused:UNUSED_PRESERVE src0_sel:WORD_1
	v_exp_f16_sdwa v41, v37 dst_sel:WORD_1 dst_unused:UNUSED_PRESERVE src0_sel:WORD_1
	v_exp_f16_sdwa v42, v38 dst_sel:WORD_1 dst_unused:UNUSED_PRESERVE src0_sel:WORD_1
	v_exp_f16_sdwa v43, v39 dst_sel:WORD_1 dst_unused:UNUSED_PRESERVE src0_sel:WORD_1
	v_pk_add_f16 v36, v56, v103
	v_pk_add_f16 v31, v31, v43
	v_pk_add_f16 v30, v30, v42
	v_pk_add_f16 v29, v29, v41
	v_pk_add_f16 v28, v28, v40
	v_pk_fma_f16 v35, v87, v43, v35
	v_pk_fma_f16 v34, v86, v42, v34
	v_pk_fma_f16 v33, v85, v41, v33
	v_pk_fma_f16 v32, v84, v40, v32
	v_pk_add_f16 v37, v57, v102
	v_pk_add_f16 v38, v58, v101
	v_pk_add_f16 v39, v59, v100
	v_exp_f16_sdwa v40, v36 dst_sel:WORD_0 dst_unused:UNUSED_PAD src0_sel:WORD_0
	v_exp_f16_sdwa v41, v37 dst_sel:WORD_0 dst_unused:UNUSED_PAD src0_sel:WORD_0
	v_exp_f16_sdwa v42, v38 dst_sel:WORD_0 dst_unused:UNUSED_PAD src0_sel:WORD_0
	v_exp_f16_sdwa v43, v39 dst_sel:WORD_0 dst_unused:UNUSED_PAD src0_sel:WORD_0
	v_exp_f16_sdwa v40, v36 dst_sel:WORD_1 dst_unused:UNUSED_PRESERVE src0_sel:WORD_1
	v_exp_f16_sdwa v41, v37 dst_sel:WORD_1 dst_unused:UNUSED_PRESERVE src0_sel:WORD_1
	v_exp_f16_sdwa v42, v38 dst_sel:WORD_1 dst_unused:UNUSED_PRESERVE src0_sel:WORD_1
	v_exp_f16_sdwa v43, v39 dst_sel:WORD_1 dst_unused:UNUSED_PRESERVE src0_sel:WORD_1
	v_pk_add_f16 v36, v68, v103
	v_pk_add_f16 v28, v28, v40
	v_pk_add_f16 v29, v29, v41
	v_pk_add_f16 v30, v30, v42
	v_pk_add_f16 v31, v31, v43
	v_pk_fma_f16 v32, v104, v40, v32
	v_pk_fma_f16 v33, v105, v41, v33
	v_pk_fma_f16 v34, v106, v42, v34
	v_pk_fma_f16 v35, v107, v43, v35
	v_pk_add_f16 v37, v69, v102
	v_pk_add_f16 v38, v70, v101
	v_pk_add_f16 v39, v71, v100
	v_exp_f16_sdwa v40, v36 dst_sel:WORD_0 dst_unused:UNUSED_PAD src0_sel:WORD_0
	v_exp_f16_sdwa v41, v37 dst_sel:WORD_0 dst_unused:UNUSED_PAD src0_sel:WORD_0
	v_exp_f16_sdwa v42, v38 dst_sel:WORD_0 dst_unused:UNUSED_PAD src0_sel:WORD_0
	v_exp_f16_sdwa v43, v39 dst_sel:WORD_0 dst_unused:UNUSED_PAD src0_sel:WORD_0
	v_exp_f16_sdwa v40, v36 dst_sel:WORD_1 dst_unused:UNUSED_PRESERVE src0_sel:WORD_1
	v_exp_f16_sdwa v41, v37 dst_sel:WORD_1 dst_unused:UNUSED_PRESERVE src0_sel:WORD_1
	v_exp_f16_sdwa v42, v38 dst_sel:WORD_1 dst_unused:UNUSED_PRESERVE src0_sel:WORD_1
	v_exp_f16_sdwa v43, v39 dst_sel:WORD_1 dst_unused:UNUSED_PRESERVE src0_sel:WORD_1
	s_nop 0
	v_pk_add_f16 v31, v31, v43
	v_pk_add_f16 v30, v30, v42
	v_pk_add_f16 v29, v29, v41
	v_pk_add_f16 v28, v28, v40
	v_pk_fma_f16 v35, v123, v43, v35
	v_pk_fma_f16 v34, v122, v42, v34
	v_pk_fma_f16 v33, v121, v41, v33
	v_pk_fma_f16 v32, v120, v40, v32
	v_pk_add_f16 v40, v72, v103
	v_pk_add_f16 v41, v73, v102
	v_pk_add_f16 v42, v74, v101
	v_pk_add_f16 v43, v75, v100
	v_exp_f16_sdwa v36, v40 dst_sel:WORD_0 dst_unused:UNUSED_PAD src0_sel:WORD_0
	v_exp_f16_sdwa v37, v41 dst_sel:WORD_0 dst_unused:UNUSED_PAD src0_sel:WORD_0
	v_exp_f16_sdwa v38, v42 dst_sel:WORD_0 dst_unused:UNUSED_PAD src0_sel:WORD_0
	v_exp_f16_sdwa v39, v43 dst_sel:WORD_0 dst_unused:UNUSED_PAD src0_sel:WORD_0
	v_exp_f16_sdwa v36, v40 dst_sel:WORD_1 dst_unused:UNUSED_PRESERVE src0_sel:WORD_1
	v_exp_f16_sdwa v37, v41 dst_sel:WORD_1 dst_unused:UNUSED_PRESERVE src0_sel:WORD_1
	v_exp_f16_sdwa v38, v42 dst_sel:WORD_1 dst_unused:UNUSED_PRESERVE src0_sel:WORD_1
	v_exp_f16_sdwa v39, v43 dst_sel:WORD_1 dst_unused:UNUSED_PRESERVE src0_sel:WORD_1
	s_nop 0
	s_load_dwordx2 s[12:13], s[0:1], 0x60
	s_branch .LBB6_76

	.amdhsa_kernel _Z7k_attn2ILi2EEv8AttnArgs
		.amdhsa_group_segment_fixed_size 0
		.amdhsa_private_segment_fixed_size 0
		.amdhsa_kernarg_size 112
		.amdhsa_user_sgpr_count 2
		.amdhsa_user_sgpr_dispatch_ptr 0
		.amdhsa_user_sgpr_queue_ptr 0
		.amdhsa_user_sgpr_kernarg_segment_ptr 1
		.amdhsa_user_sgpr_dispatch_id 0
		.amdhsa_user_sgpr_kernarg_preload_length 0
		.amdhsa_user_sgpr_kernarg_preload_offset 0
		.amdhsa_user_sgpr_private_segment_size 0
		.amdhsa_uses_dynamic_stack 0
		.amdhsa_enable_private_segment 0
		.amdhsa_system_sgpr_workgroup_id_x 1
		.amdhsa_system_sgpr_workgroup_id_y 0
		.amdhsa_system_sgpr_workgroup_id_z 0
		.amdhsa_system_sgpr_workgroup_info 0
		.amdhsa_system_vgpr_workitem_id 0
		.amdhsa_next_free_vgpr 236
		.amdhsa_next_free_sgpr 96
		.amdhsa_accum_offset 236
		.amdhsa_reserve_vcc 1
		.amdhsa_float_round_mode_32 0
		.amdhsa_float_round_mode_16_64 0
		.amdhsa_float_denorm_mode_32 3
		.amdhsa_float_denorm_mode_16_64 3
		.amdhsa_dx10_clamp 1
		.amdhsa_ieee_mode 1
		.amdhsa_fp16_overflow 0
		.amdhsa_tg_split 0
		.amdhsa_exception_fp_ieee_invalid_op 0
		.amdhsa_exception_fp_denorm_src 0
		.amdhsa_exception_fp_ieee_div_zero 0
		.amdhsa_exception_fp_ieee_overflow 0
		.amdhsa_exception_fp_ieee_underflow 0
		.amdhsa_exception_fp_ieee_inexact 0
		.amdhsa_exception_int_div_zero 0
	.end_amdhsa_kernel

amdhsa.kernels:
  - .agpr_count:     0
    .args:
      - .actual_access:  read_only
        .address_space:  global
        .offset:         0
        .size:           8
        .value_kind:     global_buffer
      - .actual_access:  read_only
        .address_space:  global
        .offset:         8
        .size:           8
        .value_kind:     global_buffer
      - .actual_access:  read_only
        .address_space:  global
        .offset:         16
        .size:           8
        .value_kind:     global_buffer
      - .actual_access:  read_only
        .address_space:  global
        .offset:         24
        .size:           8
        .value_kind:     global_buffer
      - .actual_access:  read_only
        .address_space:  global
        .offset:         32
        .size:           8
        .value_kind:     global_buffer
      - .actual_access:  read_only
        .address_space:  global
        .offset:         40
        .size:           8
        .value_kind:     global_buffer
      - .actual_access:  read_only
        .address_space:  global
        .offset:         48
        .size:           8
        .value_kind:     global_buffer
      - .actual_access:  read_only
        .address_space:  global
        .offset:         56
        .size:           8
        .value_kind:     global_buffer
      - .actual_access:  write_only
        .address_space:  global
        .offset:         64
        .size:           8
        .value_kind:     global_buffer
      - .actual_access:  write_only
        .address_space:  global
        .offset:         72
        .size:           8
        .value_kind:     global_buffer
      - .actual_access:  write_only
        .address_space:  global
        .offset:         80
        .size:           8
        .value_kind:     global_buffer
      - .actual_access:  write_only
        .address_space:  global
        .offset:         88
        .size:           8
        .value_kind:     global_buffer
    .group_segment_fixed_size: 0
    .kernarg_segment_align: 8
    .kernarg_segment_size: 96
    .language:       OpenCL C
    .language_version:
      - 2
      - 0
    .max_flat_workgroup_size: 256
    .name:           _Z8k_prep_wPKfS0_S0_S0_S0_S0_S0_S0_PDF16_PfS1_S1_
    .private_segment_fixed_size: 0
    .sgpr_count:     23
    .sgpr_spill_count: 0
    .symbol:         _Z8k_prep_wPKfS0_S0_S0_S0_S0_S0_S0_PDF16_PfS1_S1_.kd
    .uniform_work_group_size: 1
    .uses_dynamic_stack: false
    .vgpr_count:     15
    .vgpr_spill_count: 0
    .wavefront_size: 64
  - .agpr_count:     0
    .args:
      - .actual_access:  read_only
        .address_space:  global
        .offset:         0
        .size:           8
        .value_kind:     global_buffer
      - .actual_access:  read_only
        .address_space:  global
        .offset:         8
        .size:           8
        .value_kind:     global_buffer
      - .actual_access:  read_only
        .address_space:  global
        .offset:         16
        .size:           8
        .value_kind:     global_buffer
      - .actual_access:  read_only
        .address_space:  global
        .offset:         24
        .size:           8
        .value_kind:     global_buffer
      - .actual_access:  write_only
        .address_space:  global
        .offset:         32
        .size:           8
        .value_kind:     global_buffer
      - .actual_access:  read_only
        .address_space:  global
        .offset:         40
        .size:           8
        .value_kind:     global_buffer
      - .actual_access:  read_only
        .address_space:  global
        .offset:         48
        .size:           8
        .value_kind:     global_buffer
      - .actual_access:  write_only
        .address_space:  global
        .offset:         56
        .size:           8
        .value_kind:     global_buffer
      - .offset:         64
        .size:           4
        .value_kind:     by_value
      - .offset:         68
        .size:           4
        .value_kind:     by_value
    .group_segment_fixed_size: 115712
    .kernarg_segment_align: 8
    .kernarg_segment_size: 72
    .language:       OpenCL C
    .language_version:
      - 2
      - 0
    .max_flat_workgroup_size: 512
    .name:           _Z8k_stageAPKfS0_S0_S0_PDF16_PKDF16_S0_S1_ii
    .private_segment_fixed_size: 0
    .sgpr_count:     28
    .sgpr_spill_count: 0
    .symbol:         _Z8k_stageAPKfS0_S0_S0_PDF16_PKDF16_S0_S1_ii.kd
    .uniform_work_group_size: 1
    .uses_dynamic_stack: false
    .vgpr_count:     251
    .vgpr_spill_count: 0
    .wavefront_size: 64
  - .agpr_count:     112
    .args:
      - .actual_access:  read_only
        .address_space:  global
        .offset:         0
        .size:           8
        .value_kind:     global_buffer
      - .actual_access:  read_only
        .address_space:  global
        .offset:         8
        .size:           8
        .value_kind:     global_buffer
      - .actual_access:  read_only
        .address_space:  global
        .offset:         16
        .size:           8
        .value_kind:     global_buffer
      - .actual_access:  read_only
        .address_space:  global
        .offset:         24
        .size:           8
        .value_kind:     global_buffer
      - .actual_access:  read_only
        .address_space:  global
        .offset:         32
        .size:           8
        .value_kind:     global_buffer
      - .actual_access:  write_only
        .address_space:  global
        .offset:         40
        .size:           8
        .value_kind:     global_buffer
    .group_segment_fixed_size: 107712
    .kernarg_segment_align: 8
    .kernarg_segment_size: 48
    .language:       OpenCL C
    .language_version:
      - 2
      - 0
    .max_flat_workgroup_size: 256
    .name:           _Z7k_conv4PKDF16_S0_S0_PKfS2_Pf
    .private_segment_fixed_size: 0
    .sgpr_count:     36
    .sgpr_spill_count: 0
    .symbol:         _Z7k_conv4PKDF16_S0_S0_PKfS2_Pf.kd
    .uniform_work_group_size: 1
    .uses_dynamic_stack: false
    .vgpr_count:     328
    .vgpr_spill_count: 0
    .wavefront_size: 64
  - .agpr_count:     0
    .args:
      - .offset:         0
        .size:           112
        .value_kind:     by_value
      - .actual_access:  read_only
        .address_space:  global
        .offset:         112
        .size:           8
        .value_kind:     global_buffer
      - .actual_access:  read_only
        .address_space:  global
        .offset:         120
        .size:           8
        .value_kind:     global_buffer
      - .actual_access:  write_only
        .address_space:  global
        .offset:         128
        .size:           8
        .value_kind:     global_buffer
      - .offset:         136
        .size:           4
        .value_kind:     by_value
      - .offset:         140
        .size:           4
        .value_kind:     by_value
      - .offset:         144
        .size:           4
        .value_kind:     by_value
    .group_segment_fixed_size: 115712
    .kernarg_segment_align: 8
    .kernarg_segment_size: 148
    .language:       OpenCL C
    .language_version:
      - 2
      - 0
    .max_flat_workgroup_size: 512
    .name:           _Z7k_stageILi0ELi8EEv8AttnArgsPKDF16_PKfPDF16_iii
    .private_segment_fixed_size: 0
    .sgpr_count:     41
    .sgpr_spill_count: 0
    .symbol:         _Z7k_stageILi0ELi8EEv8AttnArgsPKDF16_PKfPDF16_iii.kd
    .uniform_work_group_size: 1
    .uses_dynamic_stack: false
    .vgpr_count:     255
    .vgpr_spill_count: 0
    .wavefront_size: 64
  - .agpr_count:     0
    .args:
      - .offset:         0
        .size:           112
        .value_kind:     by_value
      - .actual_access:  read_only
        .address_space:  global
        .offset:         112
        .size:           8
        .value_kind:     global_buffer
      - .actual_access:  read_only
        .address_space:  global
        .offset:         120
        .size:           8
        .value_kind:     global_buffer
      - .actual_access:  write_only
        .address_space:  global
        .offset:         128
        .size:           8
        .value_kind:     global_buffer
      - .offset:         136
        .size:           4
        .value_kind:     by_value
      - .offset:         140
        .size:           4
        .value_kind:     by_value
      - .offset:         144
        .size:           4
        .value_kind:     by_value
    .group_segment_fixed_size: 82944
    .kernarg_segment_align: 8
    .kernarg_segment_size: 148
    .language:       OpenCL C
    .language_version:
      - 2
      - 0
    .max_flat_workgroup_size: 512
    .name:           _Z7k_stageILi1ELi4EEv8AttnArgsPKDF16_PKfPDF16_iii
    .private_segment_fixed_size: 0
    .sgpr_count:     55
    .sgpr_spill_count: 0
    .symbol:         _Z7k_stageILi1ELi4EEv8AttnArgsPKDF16_PKfPDF16_iii.kd
    .uniform_work_group_size: 1
    .uses_dynamic_stack: false
    .vgpr_count:     252
    .vgpr_spill_count: 0
    .wavefront_size: 64
  - .agpr_count:     0
    .args:
      - .offset:         0
        .size:           112
        .value_kind:     by_value
      - .actual_access:  read_only
        .address_space:  global
        .offset:         112
        .size:           8
        .value_kind:     global_buffer
      - .actual_access:  read_only
        .address_space:  global
        .offset:         120
        .size:           8
        .value_kind:     global_buffer
      - .actual_access:  write_only
        .address_space:  global
        .offset:         128
        .size:           8
        .value_kind:     global_buffer
      - .offset:         136
        .size:           4
        .value_kind:     by_value
      - .offset:         140
        .size:           4
        .value_kind:     by_value
      - .offset:         144
        .size:           4
        .value_kind:     by_value
    .group_segment_fixed_size: 82944
    .kernarg_segment_align: 8
    .kernarg_segment_size: 148
    .language:       OpenCL C
    .language_version:
      - 2
      - 0
    .max_flat_workgroup_size: 512
    .name:           _Z7k_stageILi0ELi4EEv8AttnArgsPKDF16_PKfPDF16_iii
    .private_segment_fixed_size: 0
    .sgpr_count:     38
    .sgpr_spill_count: 0
    .symbol:         _Z7k_stageILi0ELi4EEv8AttnArgsPKDF16_PKfPDF16_iii.kd
    .uniform_work_group_size: 1
    .uses_dynamic_stack: false
    .vgpr_count:     230
    .vgpr_spill_count: 0
    .wavefront_size: 64
  - .agpr_count:     0
    .args:
      - .offset:         0
        .size:           112
        .value_kind:     by_value
    .group_segment_fixed_size: 0
    .kernarg_segment_align: 8
    .kernarg_segment_size: 112
    .language:       OpenCL C
    .language_version:
      - 2
      - 0
    .max_flat_workgroup_size: 512
    .name:           _Z7k_attn2ILi2EEv8AttnArgs
    .private_segment_fixed_size: 0
    .sgpr_count:     102
    .sgpr_spill_count: 0
    .symbol:         _Z7k_attn2ILi2EEv8AttnArgs.kd
    .uniform_work_group_size: 1
    .uses_dynamic_stack: false
    .vgpr_count:     236
    .vgpr_spill_count: 0
    .wavefront_size: 64
